# prologue expert-weight conversion loops also issue all 32 tile loads of a pass up front with recomputed counted waits; start-of-phase conversion slots no longer wait for their own stores before the ph
# baseline (speedup 1.0000x reference)
.LBB0_54:
	v_lshl_or_b32 v132, s12, 18, v39
	s_lshl_b32 s6, s12, 2
	v_lshl_add_u64 v[128:129], v[34:35], 0, v[132:133]
	v_or_b32_e32 v45, s6, v139
	v_bitop3_b32 v46, s6, v138, v139 bitop3:0x36
	v_add_co_u32_e32 v44, vcc, 0x1000, v128
	v_lshl_add_u32 v132, v46, 4, v38
	v_bitop3_b32 v46, v45, v138, 1 bitop3:0x36
	s_nop 1
	v_addc_co_u32_e32 v45, vcc, 0, v129, vcc
	v_add_co_u32_e32 v48, vcc, 0x2000, v128
	global_load_dwordx4 v[40:43], v[128:129], off nt
	s_nop 1
	v_addc_co_u32_e32 v49, vcc, 0, v129, vcc
	v_add_co_u32_e32 v52, vcc, 0x3000, v128
	v_lshl_add_u32 v180, v46, 4, v38
	s_nop 1
	v_addc_co_u32_e32 v53, vcc, 0, v129, vcc
	v_add_co_u32_e32 v56, vcc, 0x4000, v128
	global_load_dwordx4 v[44:47], v[44:45], off nt
	s_nop 1
	v_addc_co_u32_e32 v57, vcc, 0, v129, vcc
	v_add_co_u32_e32 v60, vcc, 0x5000, v128
	global_load_dwordx4 v[48:51], v[48:49], off nt
	s_nop 1
	global_load_dwordx4 v[52:55], v[52:53], off nt
	s_nop 1
	v_addc_co_u32_e32 v61, vcc, 0, v129, vcc
	v_add_co_u32_e32 v64, vcc, 0x6000, v128
	global_load_dwordx4 v[56:59], v[56:57], off nt
	s_nop 1
	global_load_dwordx4 v[60:63], v[60:61], off nt
	s_nop 1
	v_addc_co_u32_e32 v65, vcc, 0, v129, vcc
	v_add_co_u32_e32 v68, vcc, 0x7000, v128
	s_nop 1
	v_addc_co_u32_e32 v69, vcc, 0, v129, vcc
	v_add_co_u32_e32 v72, vcc, 0x8000, v128
	global_load_dwordx4 v[64:67], v[64:65], off nt
	s_nop 1
	global_load_dwordx4 v[68:71], v[68:69], off nt
	s_nop 1
	v_addc_co_u32_e32 v73, vcc, 0, v129, vcc
	v_add_co_u32_e32 v76, vcc, 0x9000, v128
	s_nop 1
	v_addc_co_u32_e32 v77, vcc, 0, v129, vcc
	v_add_co_u32_e32 v80, vcc, 0xa000, v128
	global_load_dwordx4 v[72:75], v[72:73], off nt
	s_nop 1
	global_load_dwordx4 v[76:79], v[76:77], off nt
	s_nop 1
	v_addc_co_u32_e32 v81, vcc, 0, v129, vcc
	v_add_co_u32_e32 v84, vcc, 0xb000, v128
	s_nop 1
	v_addc_co_u32_e32 v85, vcc, 0, v129, vcc
	v_add_co_u32_e32 v88, vcc, 0xc000, v128
	global_load_dwordx4 v[80:83], v[80:81], off nt
	s_nop 1
	global_load_dwordx4 v[84:87], v[84:85], off nt
	s_nop 1
	v_addc_co_u32_e32 v89, vcc, 0, v129, vcc
	v_add_co_u32_e32 v92, vcc, 0xd000, v128
	s_nop 1
	v_addc_co_u32_e32 v93, vcc, 0, v129, vcc
	v_add_co_u32_e32 v96, vcc, 0xe000, v128
	global_load_dwordx4 v[88:91], v[88:89], off nt
	s_nop 1
	global_load_dwordx4 v[92:95], v[92:93], off nt
	s_nop 1
	v_addc_co_u32_e32 v97, vcc, 0, v129, vcc
	v_add_co_u32_e32 v100, vcc, 0xf000, v128
	s_nop 1
	v_addc_co_u32_e32 v101, vcc, 0, v129, vcc
	v_add_co_u32_e32 v104, vcc, 0x10000, v128
	global_load_dwordx4 v[96:99], v[96:97], off nt
	s_nop 1
	global_load_dwordx4 v[100:103], v[100:101], off nt
	s_nop 1
	v_addc_co_u32_e32 v105, vcc, 0, v129, vcc
	v_add_co_u32_e32 v108, vcc, 0x11000, v128
	s_nop 1
	v_addc_co_u32_e32 v109, vcc, 0, v129, vcc
	v_add_co_u32_e32 v112, vcc, 0x12000, v128
	global_load_dwordx4 v[104:107], v[104:105], off nt
	s_nop 1
	global_load_dwordx4 v[108:111], v[108:109], off nt
	s_nop 1
	v_addc_co_u32_e32 v113, vcc, 0, v129, vcc
	v_add_co_u32_e32 v116, vcc, 0x13000, v128
	s_nop 1
	v_addc_co_u32_e32 v117, vcc, 0, v129, vcc
	v_add_co_u32_e32 v120, vcc, 0x14000, v128
	global_load_dwordx4 v[112:115], v[112:113], off nt
	s_nop 1
	global_load_dwordx4 v[116:119], v[116:117], off nt
	s_nop 1
	v_addc_co_u32_e32 v121, vcc, 0, v129, vcc
	v_add_co_u32_e32 v124, vcc, 0x15000, v128
	s_nop 1
	v_addc_co_u32_e32 v125, vcc, 0, v129, vcc
	v_add_co_u32_e32 v134, vcc, 0x16000, v128
	global_load_dwordx4 v[120:123], v[120:121], off nt
	s_nop 1
	global_load_dwordx4 v[124:127], v[124:125], off nt
	s_nop 1
	v_addc_co_u32_e32 v135, vcc, 0, v129, vcc
	v_add_co_u32_e32 v140, vcc, 0x17000, v128
	s_nop 1
	v_addc_co_u32_e32 v141, vcc, 0, v129, vcc
	v_add_co_u32_e32 v144, vcc, 0x18000, v128
	global_load_dwordx4 v[134:137], v[134:135], off nt
	s_nop 1
	global_load_dwordx4 v[140:143], v[140:141], off nt
	s_nop 1
	v_addc_co_u32_e32 v145, vcc, 0, v129, vcc
	v_add_co_u32_e32 v148, vcc, 0x19000, v128
	s_nop 1
	v_addc_co_u32_e32 v149, vcc, 0, v129, vcc
	v_add_co_u32_e32 v152, vcc, 0x1a000, v128
	global_load_dwordx4 v[144:147], v[144:145], off nt
	s_nop 1
	global_load_dwordx4 v[148:151], v[148:149], off nt
	s_nop 1
	v_addc_co_u32_e32 v153, vcc, 0, v129, vcc
	v_add_co_u32_e32 v156, vcc, 0x1b000, v128
	s_nop 1
	v_addc_co_u32_e32 v157, vcc, 0, v129, vcc
	v_add_co_u32_e32 v160, vcc, 0x1c000, v128
	global_load_dwordx4 v[152:155], v[152:153], off nt
	s_nop 1
	global_load_dwordx4 v[156:159], v[156:157], off nt
	s_nop 1
	v_addc_co_u32_e32 v161, vcc, 0, v129, vcc
	v_add_co_u32_e32 v164, vcc, 0x1d000, v128
	s_nop 1
	v_addc_co_u32_e32 v165, vcc, 0, v129, vcc
	global_load_dwordx4 v[160:163], v[160:161], off nt
	s_nop 1
	global_load_dwordx4 v[168:171], v[164:165], off nt
	v_add_co_u32_e32 v172, vcc, 0x1e000, v128
	s_nop 1
	v_addc_co_u32_e32 v173, vcc, 0, v129, vcc
	v_add_co_u32_e32 v128, vcc, 0x1f000, v128
	s_nop 1
	v_addc_co_u32_e32 v129, vcc, 0, v129, vcc
	global_load_dwordx4 v[172:175], v[172:173], off nt
	s_nop 1
	global_load_dwordx4 v[176:179], v[128:129], off nt
	s_nop 1
	s_nop 0
	s_nop 0
	s_nop 0
	s_nop 0
	s_nop 0
	s_nop 1
	v_mov_b32_e32 v6, v133
	s_nop 0
	s_nop 0
	s_nop 1
	v_mov_b32_e32 v14, v133
	s_nop 0
	s_nop 0
	s_nop 1
	v_mov_b32_e32 v22, v133
	s_nop 0
	s_nop 0
	s_nop 1
	v_mov_b32_e32 v30, v133
	s_nop 0
	s_nop 0
	s_nop 1
	v_mov_b32_e32 v7, v133
	s_nop 0
	s_nop 0
	s_nop 1
	v_mov_b32_e32 v15, v133
	s_nop 0
	s_nop 0
	s_waitcnt vmcnt(31)
	v_pk_mul_f32 v[42:43], v[42:43], s[22:23] op_sel_hi:[1,0]
	s_nop 0
	s_nop 1
	v_pk_mul_f32 v[40:41], v[40:41], s[22:23] op_sel_hi:[1,0]
	s_nop 0
	s_nop 0
	s_waitcnt vmcnt(30)
	v_pk_mul_f32 v[46:47], v[46:47], s[22:23] op_sel_hi:[1,0]
	s_nop 0
	s_nop 1
	v_pk_mul_f32 v[44:45], v[44:45], s[22:23] op_sel_hi:[1,0]
	s_nop 0
	s_nop 0
	s_nop 1
	v_cvt_pk_fp8_f32 v6, v40, v44
	s_nop 0
	s_nop 0
	s_nop 1
	v_cvt_pk_fp8_f32 v14, v41, v45
	s_nop 0
	s_nop 0
	s_nop 1
	v_cvt_pk_fp8_f32 v22, v42, v46
	s_nop 0
	s_nop 1
	v_cvt_pk_fp8_f32 v30, v43, v47
	s_nop 0
	s_nop 0
	s_nop 1
	v_mov_b32_e32 v23, v133
	v_mov_b32_e32 v31, v133
	s_waitcnt vmcnt(29)
	v_pk_mul_f32 v[50:51], v[50:51], s[22:23] op_sel_hi:[1,0]
	v_pk_mul_f32 v[48:49], v[48:49], s[22:23] op_sel_hi:[1,0]
	s_waitcnt vmcnt(28)
	v_pk_mul_f32 v[40:41], v[54:55], s[22:23] op_sel_hi:[1,0]
	v_pk_mul_f32 v[42:43], v[52:53], s[22:23] op_sel_hi:[1,0]
	s_waitcnt vmcnt(27)
	v_pk_mul_f32 v[44:45], v[58:59], s[22:23] op_sel_hi:[1,0]
	v_pk_mul_f32 v[46:47], v[56:57], s[22:23] op_sel_hi:[1,0]
	s_waitcnt vmcnt(26)
	v_pk_mul_f32 v[52:53], v[62:63], s[22:23] op_sel_hi:[1,0]
	v_pk_mul_f32 v[54:55], v[60:61], s[22:23] op_sel_hi:[1,0]
	v_mov_b32_e32 v8, v133
	v_mov_b32_e32 v16, v133
	v_mov_b32_e32 v24, v133
	v_mov_b32_e32 v32, v133
	v_cvt_pk_fp8_f32 v6, v48, v42 op_sel:[0,0,1]
	v_cvt_pk_fp8_f32 v7, v46, v54
	v_cvt_pk_fp8_f32 v14, v49, v43 op_sel:[0,0,1]
	v_cvt_pk_fp8_f32 v15, v47, v55
	v_cvt_pk_fp8_f32 v22, v50, v40 op_sel:[0,0,1]
	v_cvt_pk_fp8_f32 v23, v44, v52
	v_cvt_pk_fp8_f32 v30, v51, v41 op_sel:[0,0,1]
	v_cvt_pk_fp8_f32 v31, v45, v53
	s_waitcnt vmcnt(23)
	v_pk_mul_f32 v[44:45], v[74:75], s[22:23] op_sel_hi:[1,0]
	v_pk_mul_f32 v[46:47], v[72:73], s[22:23] op_sel_hi:[1,0]
	s_waitcnt vmcnt(22)
	v_pk_mul_f32 v[48:49], v[78:79], s[22:23] op_sel_hi:[1,0]
	v_pk_mul_f32 v[50:51], v[76:77], s[22:23] op_sel_hi:[1,0]
	v_mov_b32_e32 v17, v133
	v_mov_b32_e32 v25, v133
	v_cvt_pk_fp8_f32 v8, v46, v50
	v_cvt_pk_fp8_f32 v16, v47, v51
	v_cvt_pk_fp8_f32 v24, v44, v48
	v_cvt_pk_fp8_f32 v32, v45, v49
	s_waitcnt vmcnt(19)
	v_pk_mul_f32 v[44:45], v[90:91], s[22:23] op_sel_hi:[1,0]
	v_pk_mul_f32 v[46:47], v[88:89], s[22:23] op_sel_hi:[1,0]
	s_waitcnt vmcnt(18)
	v_pk_mul_f32 v[48:49], v[94:95], s[22:23] op_sel_hi:[1,0]
	v_pk_mul_f32 v[50:51], v[92:93], s[22:23] op_sel_hi:[1,0]
	v_cvt_pk_fp8_f32 v25, v44, v48
	v_cvt_pk_fp8_f32 v17, v47, v51
	v_pk_mul_f32 v[56:57], v[66:67], s[22:23] op_sel_hi:[1,0]
	v_pk_mul_f32 v[58:59], v[64:65], s[22:23] op_sel_hi:[1,0]
	v_pk_mul_f32 v[40:41], v[70:71], s[22:23] op_sel_hi:[1,0]
	v_pk_mul_f32 v[42:43], v[68:69], s[22:23] op_sel_hi:[1,0]
	v_mov_b32_e32 v9, v133
	v_pk_mul_f32 v[52:53], v[82:83], s[22:23] op_sel_hi:[1,0]
	v_pk_mul_f32 v[54:55], v[80:81], s[22:23] op_sel_hi:[1,0]
	v_cvt_pk_fp8_f32 v7, v58, v42 op_sel:[0,0,1]
	v_cvt_pk_fp8_f32 v15, v59, v43 op_sel:[0,0,1]
	v_cvt_pk_fp8_f32 v23, v56, v40 op_sel:[0,0,1]
	v_cvt_pk_fp8_f32 v31, v57, v41 op_sel:[0,0,1]
	v_pk_mul_f32 v[40:41], v[86:87], s[22:23] op_sel_hi:[1,0]
	v_pk_mul_f32 v[42:43], v[84:85], s[22:23] op_sel_hi:[1,0]
	v_mov_b32_e32 v33, v133
	s_waitcnt vmcnt(17)
	v_pk_mul_f32 v[56:57], v[98:99], s[22:23] op_sel_hi:[1,0]
	v_pk_mul_f32 v[58:59], v[96:97], s[22:23] op_sel_hi:[1,0]
	v_cvt_pk_fp8_f32 v8, v54, v42 op_sel:[0,0,1]
	v_cvt_pk_fp8_f32 v9, v46, v50
	v_cvt_pk_fp8_f32 v16, v55, v43 op_sel:[0,0,1]
	v_cvt_pk_fp8_f32 v24, v52, v40 op_sel:[0,0,1]
	v_cvt_pk_fp8_f32 v32, v53, v41 op_sel:[0,0,1]
	s_waitcnt vmcnt(16)
	v_pk_mul_f32 v[40:41], v[102:103], s[22:23] op_sel_hi:[1,0]
	v_pk_mul_f32 v[42:43], v[100:101], s[22:23] op_sel_hi:[1,0]
	v_cvt_pk_fp8_f32 v33, v45, v49
	v_cvt_pk_fp8_f32 v17, v59, v43 op_sel:[0,0,1]
	v_cvt_pk_fp8_f32 v25, v56, v40 op_sel:[0,0,1]
	v_mov_b32_e32 v2, v133
	v_mov_b32_e32 v10, v133
	s_waitcnt vmcnt(15)
	v_pk_mul_f32 v[46:47], v[104:105], s[22:23] op_sel_hi:[1,0]
	s_waitcnt vmcnt(14)
	v_pk_mul_f32 v[50:51], v[108:109], s[22:23] op_sel_hi:[1,0]
	v_mov_b32_e32 v3, v133
	v_mov_b32_e32 v11, v133
	v_cvt_pk_fp8_f32 v9, v58, v42 op_sel:[0,0,1]
	v_cvt_pk_fp8_f32 v2, v46, v50
	v_cvt_pk_fp8_f32 v10, v47, v51
	s_waitcnt vmcnt(11)
	v_pk_mul_f32 v[46:47], v[120:121], s[22:23] op_sel_hi:[1,0]
	s_waitcnt vmcnt(10)
	v_pk_mul_f32 v[50:51], v[124:125], s[22:23] op_sel_hi:[1,0]
	v_mov_b32_e32 v4, v133
	v_mov_b32_e32 v12, v133
	v_mov_b32_e32 v18, v133
	v_mov_b32_e32 v26, v133
	v_pk_mul_f32 v[44:45], v[106:107], s[22:23] op_sel_hi:[1,0]
	v_pk_mul_f32 v[48:49], v[110:111], s[22:23] op_sel_hi:[1,0]
	v_cvt_pk_fp8_f32 v33, v57, v41 op_sel:[0,0,1]
	v_cvt_pk_fp8_f32 v3, v46, v50
	ds_write_b128 v132, v[14:17] offset:128
	v_cvt_pk_fp8_f32 v11, v47, v51
	ds_write_b128 v132, v[22:25] offset:256
	s_waitcnt vmcnt(7)
	v_pk_mul_f32 v[16:17], v[144:145], s[22:23] op_sel_hi:[1,0]
	s_waitcnt vmcnt(6)
	v_pk_mul_f32 v[24:25], v[148:149], s[22:23] op_sel_hi:[1,0]
	v_mov_b32_e32 v5, v133
	v_mov_b32_e32 v19, v133
	v_mov_b32_e32 v27, v133
	v_cvt_pk_fp8_f32 v18, v44, v48
	v_cvt_pk_fp8_f32 v26, v45, v49
	v_pk_mul_f32 v[44:45], v[122:123], s[22:23] op_sel_hi:[1,0]
	v_pk_mul_f32 v[48:49], v[126:127], s[22:23] op_sel_hi:[1,0]
	v_cvt_pk_fp8_f32 v4, v16, v24
	v_cvt_pk_fp8_f32 v12, v17, v25
	s_waitcnt vmcnt(3)
	v_pk_mul_f32 v[16:17], v[160:161], s[22:23] op_sel_hi:[1,0]
	s_waitcnt vmcnt(2)
	v_pk_mul_f32 v[24:25], v[168:169], s[22:23] op_sel_hi:[1,0]
	v_mov_b32_e32 v13, v133
	v_mov_b32_e32 v20, v133
	v_mov_b32_e32 v28, v133
	v_cvt_pk_fp8_f32 v19, v44, v48
	v_cvt_pk_fp8_f32 v27, v45, v49
	v_pk_mul_f32 v[14:15], v[146:147], s[22:23] op_sel_hi:[1,0]
	v_pk_mul_f32 v[22:23], v[150:151], s[22:23] op_sel_hi:[1,0]
	v_cvt_pk_fp8_f32 v5, v16, v24
	v_mov_b32_e32 v21, v133
	v_pk_mul_f32 v[58:59], v[134:135], s[22:23] op_sel_hi:[1,0]
	ds_write_b128 v132, v[6:9]
	v_pk_mul_f32 v[8:9], v[140:141], s[22:23] op_sel_hi:[1,0]
	v_cvt_pk_fp8_f32 v20, v14, v22
	v_cvt_pk_fp8_f32 v28, v15, v23
	v_pk_mul_f32 v[14:15], v[162:163], s[22:23] op_sel_hi:[1,0]
	v_pk_mul_f32 v[22:23], v[170:171], s[22:23] op_sel_hi:[1,0]
	v_cvt_pk_fp8_f32 v13, v17, v25
	v_mov_b32_e32 v29, v133
	v_pk_mul_f32 v[54:55], v[112:113], s[22:23] op_sel_hi:[1,0]
	v_pk_mul_f32 v[42:43], v[116:117], s[22:23] op_sel_hi:[1,0]
	ds_write_b128 v132, v[30:33] offset:384
	v_pk_mul_f32 v[32:33], v[152:153], s[22:23] op_sel_hi:[1,0]
	v_cvt_pk_fp8_f32 v3, v58, v8 op_sel:[0,0,1]
	v_cvt_pk_fp8_f32 v11, v59, v9 op_sel:[0,0,1]
	v_pk_mul_f32 v[8:9], v[156:157], s[22:23] op_sel_hi:[1,0]
	v_cvt_pk_fp8_f32 v21, v14, v22
	v_pk_mul_f32 v[56:57], v[136:137], s[22:23] op_sel_hi:[1,0]
	v_cvt_pk_fp8_f32 v2, v54, v42 op_sel:[0,0,1]
	v_cvt_pk_fp8_f32 v10, v55, v43 op_sel:[0,0,1]
	v_pk_mul_f32 v[6:7], v[142:143], s[22:23] op_sel_hi:[1,0]
	s_waitcnt vmcnt(1)
	v_pk_mul_f32 v[42:43], v[172:173], s[22:23] op_sel_hi:[1,0]
	v_cvt_pk_fp8_f32 v4, v32, v8 op_sel:[0,0,1]
	v_cvt_pk_fp8_f32 v12, v33, v9 op_sel:[0,0,1]
	v_cvt_pk_fp8_f32 v29, v15, v23
	s_waitcnt vmcnt(0)
	v_pk_mul_f32 v[8:9], v[176:177], s[22:23] op_sel_hi:[1,0]
	v_pk_mul_f32 v[52:53], v[114:115], s[22:23] op_sel_hi:[1,0]
	v_pk_mul_f32 v[40:41], v[118:119], s[22:23] op_sel_hi:[1,0]
	v_pk_mul_f32 v[30:31], v[154:155], s[22:23] op_sel_hi:[1,0]
	v_cvt_pk_fp8_f32 v19, v56, v6 op_sel:[0,0,1]
	v_cvt_pk_fp8_f32 v27, v57, v7 op_sel:[0,0,1]
	v_pk_mul_f32 v[6:7], v[158:159], s[22:23] op_sel_hi:[1,0]
	v_cvt_pk_fp8_f32 v5, v42, v8 op_sel:[0,0,1]
	v_cvt_pk_fp8_f32 v18, v52, v40 op_sel:[0,0,1]
	v_cvt_pk_fp8_f32 v26, v53, v41 op_sel:[0,0,1]
	v_pk_mul_f32 v[40:41], v[174:175], s[22:23] op_sel_hi:[1,0]
	v_cvt_pk_fp8_f32 v20, v30, v6 op_sel:[0,0,1]
	v_cvt_pk_fp8_f32 v28, v31, v7 op_sel:[0,0,1]
	v_pk_mul_f32 v[6:7], v[178:179], s[22:23] op_sel_hi:[1,0]
	v_cvt_pk_fp8_f32 v13, v43, v9 op_sel:[0,0,1]
	s_and_b64 s[0:1], exec, s[10:11]
	v_cvt_pk_fp8_f32 v21, v40, v6 op_sel:[0,0,1]
	s_mov_b32 s12, 1
	s_mov_b64 s[10:11], 0
	v_cvt_pk_fp8_f32 v29, v41, v7 op_sel:[0,0,1]
	s_mov_b64 vcc, s[0:1]
	ds_write_b128 v180, v[2:5]
	ds_write_b128 v180, v[10:13] offset:128
	ds_write_b128 v180, v[18:21] offset:256
	ds_write_b128 v180, v[26:29] offset:384
	s_cbranch_vccnz .LBB0_54
	s_lshl_b32 s0, s5, 10
	s_or_b32 s0, s0, s9
	s_mulk_i32 s0, 0xb00
	s_add_u32 s0, s2, s0
	s_addc_u32 s1, s38, 0
	s_waitcnt lgkmcnt(0)
	v_mov_b32_e32 v14, v131
	s_add_u32 s0, s0, s4
	s_addc_u32 s1, s1, s7
	v_lshlrev_b32_e32 v2, 4, v14
	v_and_b32_e32 v132, 0x70, v2
	v_ashrrev_i32_e32 v15, 3, v14
	v_lshl_add_u64 v[2:3], s[0:1], 0, v[132:133]
	s_mov_b64 s[0:1], 0xbc00000
	v_lshl_add_u64 v[10:11], v[2:3], 0, s[0:1]
	v_lshrrev_b32_e32 v3, 2, v15
	v_add_u32_e32 v17, 8, v15
	v_xor_b32_e32 v3, v3, v14
	v_lshrrev_b32_e32 v7, 2, v17
	v_lshlrev_b32_e32 v3, 4, v3
	v_xor_b32_e32 v7, v7, v14
	v_lshlrev_b32_e32 v2, 7, v15
	v_and_b32_e32 v16, 0x70, v3
	v_lshlrev_b32_e32 v7, 4, v7
	v_add3_u32 v2, s29, v2, v16
	v_lshlrev_b32_e32 v6, 7, v17
	v_and_b32_e32 v7, 0x70, v7
	ds_read_b128 v[2:5], v2
	v_add3_u32 v6, s29, v6, v7
	ds_read_b128 v[6:9], v6
	s_movk_i32 s4, 0xb00
	v_mad_i64_i32 v[12:13], s[0:1], v15, s4, v[10:11]
	s_waitcnt lgkmcnt(1)
	global_store_dwordx4 v[12:13], v[2:5], off nt
	v_add_u32_e32 v12, 16, v15
	s_nop 0
	v_mad_i64_i32 v[2:3], s[0:1], v17, s4, v[10:11]
	s_waitcnt lgkmcnt(0)
	global_store_dwordx4 v[2:3], v[6:9], off nt
	v_lshrrev_b32_e32 v3, 2, v12
	v_add_u32_e32 v17, 24, v15
	v_xor_b32_e32 v3, v3, v14
	v_lshrrev_b32_e32 v7, 2, v17
	v_lshlrev_b32_e32 v3, 4, v3
	v_xor_b32_e32 v7, v7, v14
	v_lshlrev_b32_e32 v2, 7, v12
	v_and_b32_e32 v3, 0x70, v3
	v_lshlrev_b32_e32 v7, 4, v7
	v_add3_u32 v2, s29, v2, v3
	v_lshlrev_b32_e32 v6, 7, v17
	v_and_b32_e32 v7, 0x70, v7
	ds_read_b128 v[2:5], v2
	v_add3_u32 v6, s29, v6, v7
	ds_read_b128 v[6:9], v6
	v_mad_i64_i32 v[12:13], s[0:1], v12, s4, v[10:11]
	s_waitcnt lgkmcnt(1)
	global_store_dwordx4 v[12:13], v[2:5], off nt
	v_add_u32_e32 v12, 32, v15
	s_nop 0
	v_mad_i64_i32 v[2:3], s[0:1], v17, s4, v[10:11]
	v_add_u32_e32 v17, 40, v15
	s_waitcnt lgkmcnt(0)
	global_store_dwordx4 v[2:3], v[6:9], off nt
	v_lshlrev_b32_e32 v2, 7, v12
	v_add3_u32 v2, s29, v2, v16
	v_lshrrev_b32_e32 v7, 2, v17
	v_xor_b32_e32 v7, v7, v14
	v_lshlrev_b32_e32 v7, 4, v7
	v_lshlrev_b32_e32 v6, 7, v17
	v_and_b32_e32 v7, 0x70, v7
	ds_read_b128 v[2:5], v2
	v_add3_u32 v6, s29, v6, v7
	ds_read_b128 v[6:9], v6
	v_mad_i64_i32 v[12:13], s[0:1], v12, s4, v[10:11]
	s_waitcnt lgkmcnt(1)
	global_store_dwordx4 v[12:13], v[2:5], off nt
	v_add_u32_e32 v12, 48, v15
	s_nop 0
	v_mad_i64_i32 v[2:3], s[0:1], v17, s4, v[10:11]
	s_waitcnt lgkmcnt(0)
	global_store_dwordx4 v[2:3], v[6:9], off nt
	v_lshrrev_b32_e32 v3, 2, v12
	v_add_u32_e32 v17, 56, v15
	v_xor_b32_e32 v3, v3, v14
	v_lshrrev_b32_e32 v7, 2, v17
	v_lshlrev_b32_e32 v3, 4, v3
	v_xor_b32_e32 v7, v7, v14
	v_lshlrev_b32_e32 v2, 7, v12
	v_and_b32_e32 v3, 0x70, v3
	v_lshlrev_b32_e32 v7, 4, v7
	v_add3_u32 v2, s29, v2, v3
	v_lshlrev_b32_e32 v6, 7, v17
	v_and_b32_e32 v7, 0x70, v7
	ds_read_b128 v[2:5], v2
	v_add3_u32 v6, s29, v6, v7
	ds_read_b128 v[6:9], v6
	v_mad_i64_i32 v[12:13], s[0:1], v12, s4, v[10:11]
	s_waitcnt lgkmcnt(1)
	global_store_dwordx4 v[12:13], v[2:5], off nt
	v_add_u32_e32 v12, 64, v15
	s_nop 0
	v_mad_i64_i32 v[2:3], s[0:1], v17, s4, v[10:11]
	v_add_u32_e32 v17, 0x48, v15
	s_waitcnt lgkmcnt(0)
	global_store_dwordx4 v[2:3], v[6:9], off nt
	v_lshlrev_b32_e32 v2, 7, v12
	v_add3_u32 v2, s29, v2, v16
	v_lshrrev_b32_e32 v7, 2, v17
	v_xor_b32_e32 v7, v7, v14
	v_lshlrev_b32_e32 v7, 4, v7
	v_lshlrev_b32_e32 v6, 7, v17
	v_and_b32_e32 v7, 0x70, v7
	ds_read_b128 v[2:5], v2
	v_add3_u32 v6, s29, v6, v7
	ds_read_b128 v[6:9], v6
	v_mad_i64_i32 v[12:13], s[0:1], v12, s4, v[10:11]
	s_waitcnt lgkmcnt(1)
	global_store_dwordx4 v[12:13], v[2:5], off nt
	v_add_u32_e32 v12, 0x50, v15
	s_nop 0
	v_mad_i64_i32 v[2:3], s[0:1], v17, s4, v[10:11]
	s_waitcnt lgkmcnt(0)
	global_store_dwordx4 v[2:3], v[6:9], off nt
	v_lshrrev_b32_e32 v3, 2, v12
	v_add_u32_e32 v17, 0x58, v15
	v_xor_b32_e32 v3, v3, v14
	v_lshrrev_b32_e32 v7, 2, v17
	v_lshlrev_b32_e32 v3, 4, v3
	v_xor_b32_e32 v7, v7, v14
	v_lshlrev_b32_e32 v2, 7, v12
	v_and_b32_e32 v3, 0x70, v3
	v_lshlrev_b32_e32 v7, 4, v7
	v_add3_u32 v2, s29, v2, v3
	v_lshlrev_b32_e32 v6, 7, v17
	v_and_b32_e32 v7, 0x70, v7
	ds_read_b128 v[2:5], v2
	v_add3_u32 v6, s29, v6, v7
	ds_read_b128 v[6:9], v6
	v_mad_i64_i32 v[12:13], s[0:1], v12, s4, v[10:11]
	s_waitcnt lgkmcnt(1)
	global_store_dwordx4 v[12:13], v[2:5], off nt
	v_add_u32_e32 v12, 0x60, v15
	s_nop 0
	v_mad_i64_i32 v[2:3], s[0:1], v17, s4, v[10:11]
	s_waitcnt lgkmcnt(0)
	global_store_dwordx4 v[2:3], v[6:9], off nt
	v_lshlrev_b32_e32 v2, 7, v12
	v_add3_u32 v2, s29, v2, v16
	v_add_u32_e32 v16, 0x68, v15
	v_lshrrev_b32_e32 v7, 2, v16
	v_xor_b32_e32 v7, v7, v14
	v_lshlrev_b32_e32 v7, 4, v7
	v_lshlrev_b32_e32 v6, 7, v16
	v_and_b32_e32 v7, 0x70, v7
	ds_read_b128 v[2:5], v2
	v_add3_u32 v6, s29, v6, v7
	ds_read_b128 v[6:9], v6
	v_mad_i64_i32 v[12:13], s[0:1], v12, s4, v[10:11]
	s_waitcnt lgkmcnt(1)
	global_store_dwordx4 v[12:13], v[2:5], off nt
	v_add_u32_e32 v12, 0x70, v15
	v_add_u32_e32 v15, 0x78, v15
	v_mad_i64_i32 v[2:3], s[0:1], v16, s4, v[10:11]
	s_waitcnt lgkmcnt(0)
	global_store_dwordx4 v[2:3], v[6:9], off nt
	v_lshrrev_b32_e32 v3, 2, v12
	v_xor_b32_e32 v3, v3, v14
	v_lshrrev_b32_e32 v7, 2, v15
	v_lshlrev_b32_e32 v3, 4, v3
	v_xor_b32_e32 v7, v7, v14
	v_lshlrev_b32_e32 v2, 7, v12
	v_and_b32_e32 v3, 0x70, v3
	v_lshlrev_b32_e32 v7, 4, v7
	v_add3_u32 v2, s29, v2, v3
	v_lshlrev_b32_e32 v6, 7, v15
	v_and_b32_e32 v7, 0x70, v7
	ds_read_b128 v[2:5], v2
	v_add3_u32 v6, s29, v6, v7
	ds_read_b128 v[6:9], v6
	v_mad_i64_i32 v[12:13], s[0:1], v12, s4, v[10:11]
	s_waitcnt lgkmcnt(1)
	global_store_dwordx4 v[12:13], v[2:5], off nt
	s_nop 1
	v_mad_i64_i32 v[2:3], s[0:1], v15, s4, v[10:11]
	s_waitcnt lgkmcnt(0)
	global_store_dwordx4 v[2:3], v[6:9], off nt
	s_waitcnt lgkmcnt(0)
	s_mov_b64 s[0:1], 0

.LBB0_62:
	v_or_b32_e32 v2, s5, v140
	v_mul_u32_u24_e32 v132, 0x2c00, v2
	v_lshl_add_u64 v[10:11], v[134:135], 0, v[132:133]
	v_add_co_u32_e32 v2, vcc, 0x2000, v10
	s_mov_b32 s5, 0x21000
	s_nop 1
	v_addc_co_u32_e32 v3, vcc, 0, v11, vcc
	global_load_dwordx4 v[126:129], v[10:11], off nt
	global_load_dwordx4 v[118:121], v[2:3], off offset:3072 nt
	v_add_co_u32_e32 v2, vcc, 0x5000, v10
	s_nop 1
	v_addc_co_u32_e32 v3, vcc, 0, v11, vcc
	v_add_co_u32_e32 v4, vcc, 0x8000, v10
	s_nop 1
	v_addc_co_u32_e32 v5, vcc, 0, v11, vcc
	global_load_dwordx4 v[122:125], v[2:3], off offset:2048 nt
	global_load_dwordx4 v[110:113], v[4:5], off offset:1024 nt
	v_add_co_u32_e32 v2, vcc, 0xb000, v10
	s_nop 1
	v_addc_co_u32_e32 v3, vcc, 0, v11, vcc
	v_add_co_u32_e32 v4, vcc, 0xd000, v10
	s_nop 1
	v_addc_co_u32_e32 v5, vcc, 0, v11, vcc
	global_load_dwordx4 v[114:117], v[2:3], off nt
	global_load_dwordx4 v[102:105], v[4:5], off offset:3072 nt
	v_add_co_u32_e32 v2, vcc, 0x10000, v10
	s_nop 1
	v_addc_co_u32_e32 v3, vcc, 0, v11, vcc
	v_add_co_u32_e32 v4, vcc, 0x13000, v10
	s_nop 1
	v_addc_co_u32_e32 v5, vcc, 0, v11, vcc
	global_load_dwordx4 v[106:109], v[2:3], off offset:2048 nt
	global_load_dwordx4 v[94:97], v[4:5], off offset:1024 nt
	v_add_co_u32_e32 v2, vcc, 0x16000, v10
	s_nop 1
	v_addc_co_u32_e32 v3, vcc, 0, v11, vcc
	v_add_co_u32_e32 v4, vcc, 0x18000, v10
	s_nop 1
	v_addc_co_u32_e32 v5, vcc, 0, v11, vcc
	global_load_dwordx4 v[98:101], v[2:3], off nt
	global_load_dwordx4 v[86:89], v[4:5], off offset:3072 nt
	v_add_co_u32_e32 v2, vcc, 0x1b000, v10
	s_nop 1
	v_addc_co_u32_e32 v3, vcc, 0, v11, vcc
	v_add_co_u32_e32 v4, vcc, 0x1e000, v10
	s_nop 1
	v_addc_co_u32_e32 v5, vcc, 0, v11, vcc
	global_load_dwordx4 v[90:93], v[2:3], off offset:2048 nt
	global_load_dwordx4 v[78:81], v[4:5], off offset:1024 nt
	v_add_co_u32_e32 v2, vcc, s5, v10
	s_nop 1
	v_addc_co_u32_e32 v3, vcc, 0, v11, vcc
	v_add_co_u32_e32 v4, vcc, 0x23000, v10
	s_nop 1
	v_addc_co_u32_e32 v5, vcc, 0, v11, vcc
	global_load_dwordx4 v[82:85], v[2:3], off nt
	global_load_dwordx4 v[70:73], v[4:5], off offset:3072 nt
	v_add_co_u32_e32 v2, vcc, 0x26000, v10
	s_nop 1
	v_addc_co_u32_e32 v3, vcc, 0, v11, vcc
	v_add_co_u32_e32 v4, vcc, 0x29000, v10
	s_nop 1
	v_addc_co_u32_e32 v5, vcc, 0, v11, vcc
	global_load_dwordx4 v[74:77], v[2:3], off offset:2048 nt
	global_load_dwordx4 v[62:65], v[4:5], off offset:1024 nt
	v_add_co_u32_e32 v2, vcc, 0x2c000, v10
	s_nop 1
	v_addc_co_u32_e32 v3, vcc, 0, v11, vcc
	v_add_co_u32_e32 v4, vcc, 0x2e000, v10
	s_nop 1
	v_addc_co_u32_e32 v5, vcc, 0, v11, vcc
	global_load_dwordx4 v[66:69], v[2:3], off nt
	global_load_dwordx4 v[54:57], v[4:5], off offset:3072 nt
	v_add_co_u32_e32 v2, vcc, 0x31000, v10
	s_nop 1
	v_addc_co_u32_e32 v3, vcc, 0, v11, vcc
	v_add_co_u32_e32 v4, vcc, 0x34000, v10
	s_nop 1
	v_addc_co_u32_e32 v5, vcc, 0, v11, vcc
	global_load_dwordx4 v[58:61], v[2:3], off offset:2048 nt
	global_load_dwordx4 v[46:49], v[4:5], off offset:1024 nt
	v_add_co_u32_e32 v2, vcc, 0x37000, v10
	s_nop 1
	v_addc_co_u32_e32 v3, vcc, 0, v11, vcc
	v_add_co_u32_e32 v4, vcc, 0x39000, v10
	s_nop 1
	v_addc_co_u32_e32 v5, vcc, 0, v11, vcc
	global_load_dwordx4 v[50:53], v[2:3], off nt
	global_load_dwordx4 v[38:41], v[4:5], off offset:3072 nt
	v_add_co_u32_e32 v2, vcc, 0x3c000, v10
	s_nop 1
	v_addc_co_u32_e32 v3, vcc, 0, v11, vcc
	v_add_co_u32_e32 v4, vcc, 0x3f000, v10
	s_nop 1
	v_addc_co_u32_e32 v5, vcc, 0, v11, vcc
	global_load_dwordx4 v[42:45], v[2:3], off offset:2048 nt
	global_load_dwordx4 v[30:33], v[4:5], off offset:1024 nt
	v_add_co_u32_e32 v2, vcc, 0x42000, v10
	s_nop 1
	v_addc_co_u32_e32 v3, vcc, 0, v11, vcc
	v_add_co_u32_e32 v4, vcc, 0x44000, v10
	s_nop 1
	v_addc_co_u32_e32 v5, vcc, 0, v11, vcc
	global_load_dwordx4 v[34:37], v[2:3], off nt
	global_load_dwordx4 v[26:29], v[4:5], off offset:3072 nt
	v_add_co_u32_e32 v2, vcc, 0x47000, v10
	s_nop 1
	v_addc_co_u32_e32 v3, vcc, 0, v11, vcc
	v_add_co_u32_e32 v4, vcc, 0x4a000, v10
	s_nop 1
	v_addc_co_u32_e32 v5, vcc, 0, v11, vcc
	global_load_dwordx4 v[22:25], v[2:3], off offset:2048 nt
	global_load_dwordx4 v[14:17], v[4:5], off offset:1024 nt
	v_add_co_u32_e32 v2, vcc, 0x4d000, v10
	s_nop 1
	v_addc_co_u32_e32 v3, vcc, 0, v11, vcc
	v_add_co_u32_e32 v4, vcc, 0x4f000, v10
	s_nop 1
	v_addc_co_u32_e32 v5, vcc, 0, v11, vcc
	global_load_dwordx4 v[6:9], v[2:3], off nt
	s_nop 1
	global_load_dwordx4 v[2:5], v[4:5], off offset:3072 nt
	v_add_co_u32_e32 v12, vcc, 0x52000, v10
	s_nop 1
	v_addc_co_u32_e32 v13, vcc, 0, v11, vcc
	v_add_co_u32_e32 v10, vcc, 0x55000, v10
	s_nop 1
	v_addc_co_u32_e32 v11, vcc, 0, v11, vcc
	global_load_dwordx4 v[18:21], v[12:13], off offset:2048 nt
	s_nop 1
	global_load_dwordx4 v[10:13], v[10:11], off offset:1024 nt
	s_nop 1
	s_nop 0
	s_waitcnt vmcnt(32)
	ds_bpermute_b32 v132, v141, v175
	s_nop 1
	ds_bpermute_b32 v136, v142, v175
	s_nop 0
	s_nop 1
	ds_bpermute_b32 v176, v143, v175
	s_nop 0
	s_waitcnt lgkmcnt(2)
	v_mul_f32_e32 v132, s40, v132
	s_nop 1
	ds_bpermute_b32 v177, v144, v175
	s_nop 0
	s_nop 1
	s_lshl_b32 s4, s4, 2
	s_nop 0
	s_nop 1
	s_xor_b64 s[6:7], s[16:17], -1
	s_nop 0
	s_nop 1
	s_mov_b64 s[16:17], 0
	s_nop 0
	s_waitcnt vmcnt(31)
	v_pk_mul_f32 v[128:129], v[128:129], v[132:133] op_sel_hi:[1,0]
	s_nop 1
	v_pk_mul_f32 v[126:127], v[126:127], v[132:133] op_sel_hi:[1,0]
	s_nop 0
	s_waitcnt lgkmcnt(2)
	v_mul_f32_e32 v132, s40, v136
	s_waitcnt vmcnt(30)
	v_pk_mul_f32 v[120:121], v[120:121], v[132:133] op_sel_hi:[1,0]
	s_nop 1
	v_pk_mul_f32 v[136:137], v[118:119], v[132:133] op_sel_hi:[1,0]
	s_nop 0
	s_waitcnt lgkmcnt(1)
	v_mul_f32_e32 v132, s40, v176
	s_waitcnt vmcnt(29)
	v_pk_mul_f32 v[118:119], v[124:125], v[132:133] op_sel_hi:[1,0]
	s_nop 1
	v_pk_mul_f32 v[122:123], v[122:123], v[132:133] op_sel_hi:[1,0]
	s_nop 0
	s_nop 1
	ds_bpermute_b32 v132, v145, v175
	s_nop 0
	s_waitcnt lgkmcnt(1)
	v_mul_f32_e32 v124, s40, v177
	s_waitcnt lgkmcnt(0)
	v_mul_f32_e32 v132, s40, v132
	s_waitcnt vmcnt(28)
	v_pk_mul_f32 v[112:113], v[112:113], v[124:125] op_sel_hi:[1,0]
	s_nop 1
	v_pk_mul_f32 v[124:125], v[110:111], v[124:125] op_sel_hi:[1,0]
	s_nop 0
	s_nop 1
	ds_bpermute_b32 v176, v146, v175
	s_nop 0
	s_waitcnt vmcnt(27)
	v_pk_mul_f32 v[110:111], v[116:117], v[132:133] op_sel_hi:[1,0]
	s_nop 1
	v_pk_mul_f32 v[114:115], v[114:115], v[132:133] op_sel_hi:[1,0]
	s_nop 0
	s_nop 1
	ds_bpermute_b32 v132, v147, v175
	s_nop 0
	s_waitcnt lgkmcnt(1)
	v_mul_f32_e32 v116, s40, v176
	s_waitcnt lgkmcnt(0)
	v_mul_f32_e32 v132, s40, v132
	s_waitcnt vmcnt(26)
	v_pk_mul_f32 v[104:105], v[104:105], v[116:117] op_sel_hi:[1,0]
	s_nop 0
	s_nop 1
	v_pk_mul_f32 v[116:117], v[102:103], v[116:117] op_sel_hi:[1,0]
	s_nop 0
	s_nop 1
	ds_bpermute_b32 v176, v148, v175
	s_nop 0
	s_nop 0
	s_waitcnt vmcnt(25)
	v_pk_mul_f32 v[102:103], v[108:109], v[132:133] op_sel_hi:[1,0]
	v_pk_mul_f32 v[106:107], v[106:107], v[132:133] op_sel_hi:[1,0]
	ds_bpermute_b32 v132, v149, v175
	s_waitcnt lgkmcnt(1)
	v_mul_f32_e32 v108, s40, v176
	s_waitcnt vmcnt(24)
	v_pk_mul_f32 v[96:97], v[96:97], v[108:109] op_sel_hi:[1,0]
	v_pk_mul_f32 v[108:109], v[94:95], v[108:109] op_sel_hi:[1,0]
	ds_bpermute_b32 v176, v150, v175
	s_waitcnt lgkmcnt(1)
	v_mul_f32_e32 v132, s40, v132
	s_waitcnt vmcnt(23)
	v_pk_mul_f32 v[94:95], v[100:101], v[132:133] op_sel_hi:[1,0]
	v_pk_mul_f32 v[98:99], v[98:99], v[132:133] op_sel_hi:[1,0]
	ds_bpermute_b32 v132, v151, v175
	s_waitcnt lgkmcnt(1)
	v_mul_f32_e32 v100, s40, v176
	s_waitcnt vmcnt(22)
	v_pk_mul_f32 v[88:89], v[88:89], v[100:101] op_sel_hi:[1,0]
	v_pk_mul_f32 v[100:101], v[86:87], v[100:101] op_sel_hi:[1,0]
	ds_bpermute_b32 v176, v152, v175
	s_waitcnt lgkmcnt(1)
	v_mul_f32_e32 v132, s40, v132
	s_waitcnt vmcnt(21)
	v_pk_mul_f32 v[86:87], v[92:93], v[132:133] op_sel_hi:[1,0]
	v_pk_mul_f32 v[90:91], v[90:91], v[132:133] op_sel_hi:[1,0]
	ds_bpermute_b32 v132, v153, v175
	s_waitcnt lgkmcnt(1)
	v_mul_f32_e32 v92, s40, v176
	s_waitcnt vmcnt(20)
	v_pk_mul_f32 v[80:81], v[80:81], v[92:93] op_sel_hi:[1,0]
	v_pk_mul_f32 v[92:93], v[78:79], v[92:93] op_sel_hi:[1,0]
	ds_bpermute_b32 v176, v154, v175
	s_waitcnt lgkmcnt(1)
	v_mul_f32_e32 v132, s40, v132
	s_waitcnt vmcnt(19)
	v_pk_mul_f32 v[78:79], v[84:85], v[132:133] op_sel_hi:[1,0]
	v_pk_mul_f32 v[82:83], v[82:83], v[132:133] op_sel_hi:[1,0]
	ds_bpermute_b32 v132, v155, v175
	s_waitcnt lgkmcnt(1)
	v_mul_f32_e32 v84, s40, v176
	s_waitcnt vmcnt(18)
	v_pk_mul_f32 v[72:73], v[72:73], v[84:85] op_sel_hi:[1,0]
	v_pk_mul_f32 v[84:85], v[70:71], v[84:85] op_sel_hi:[1,0]
	ds_bpermute_b32 v176, v156, v175
	s_waitcnt lgkmcnt(1)
	v_mul_f32_e32 v132, s40, v132
	s_waitcnt vmcnt(17)
	v_pk_mul_f32 v[70:71], v[76:77], v[132:133] op_sel_hi:[1,0]
	v_pk_mul_f32 v[74:75], v[74:75], v[132:133] op_sel_hi:[1,0]
	ds_bpermute_b32 v132, v157, v175
	s_waitcnt lgkmcnt(1)
	v_mul_f32_e32 v76, s40, v176
	s_waitcnt vmcnt(16)
	v_pk_mul_f32 v[64:65], v[64:65], v[76:77] op_sel_hi:[1,0]
	v_pk_mul_f32 v[76:77], v[62:63], v[76:77] op_sel_hi:[1,0]
	ds_bpermute_b32 v176, v158, v175
	s_waitcnt lgkmcnt(1)
	v_mul_f32_e32 v132, s40, v132
	s_waitcnt vmcnt(15)
	v_pk_mul_f32 v[62:63], v[68:69], v[132:133] op_sel_hi:[1,0]
	v_pk_mul_f32 v[66:67], v[66:67], v[132:133] op_sel_hi:[1,0]
	ds_bpermute_b32 v132, v159, v175
	s_waitcnt lgkmcnt(1)
	v_mul_f32_e32 v68, s40, v176
	s_waitcnt vmcnt(14)
	v_pk_mul_f32 v[56:57], v[56:57], v[68:69] op_sel_hi:[1,0]
	v_pk_mul_f32 v[68:69], v[54:55], v[68:69] op_sel_hi:[1,0]
	ds_bpermute_b32 v176, v160, v175
	s_waitcnt lgkmcnt(1)
	v_mul_f32_e32 v132, s40, v132
	s_waitcnt vmcnt(13)
	v_pk_mul_f32 v[54:55], v[60:61], v[132:133] op_sel_hi:[1,0]
	v_pk_mul_f32 v[58:59], v[58:59], v[132:133] op_sel_hi:[1,0]
	ds_bpermute_b32 v132, v161, v175
	s_waitcnt lgkmcnt(1)
	v_mul_f32_e32 v60, s40, v176
	s_waitcnt vmcnt(12)
	v_pk_mul_f32 v[48:49], v[48:49], v[60:61] op_sel_hi:[1,0]
	v_pk_mul_f32 v[60:61], v[46:47], v[60:61] op_sel_hi:[1,0]
	ds_bpermute_b32 v176, v162, v175
	s_waitcnt lgkmcnt(1)
	v_mul_f32_e32 v132, s40, v132
	s_waitcnt vmcnt(11)
	v_pk_mul_f32 v[46:47], v[52:53], v[132:133] op_sel_hi:[1,0]
	v_pk_mul_f32 v[50:51], v[50:51], v[132:133] op_sel_hi:[1,0]
	ds_bpermute_b32 v132, v163, v175
	s_waitcnt lgkmcnt(1)
	v_mul_f32_e32 v52, s40, v176
	s_waitcnt vmcnt(10)
	v_pk_mul_f32 v[40:41], v[40:41], v[52:53] op_sel_hi:[1,0]
	v_pk_mul_f32 v[52:53], v[38:39], v[52:53] op_sel_hi:[1,0]
	ds_bpermute_b32 v176, v164, v175
	s_waitcnt lgkmcnt(1)
	v_mul_f32_e32 v132, s40, v132
	s_waitcnt vmcnt(9)
	v_pk_mul_f32 v[38:39], v[44:45], v[132:133] op_sel_hi:[1,0]
	v_pk_mul_f32 v[42:43], v[42:43], v[132:133] op_sel_hi:[1,0]
	ds_bpermute_b32 v132, v165, v175
	s_waitcnt lgkmcnt(1)
	v_mul_f32_e32 v44, s40, v176
	ds_bpermute_b32 v176, v167, v175
	s_waitcnt vmcnt(8)
	v_pk_mul_f32 v[32:33], v[32:33], v[44:45] op_sel_hi:[1,0]
	v_pk_mul_f32 v[44:45], v[30:31], v[44:45] op_sel_hi:[1,0]
	s_waitcnt lgkmcnt(1)
	v_mul_f32_e32 v132, s40, v132
	s_waitcnt vmcnt(7)
	v_pk_mul_f32 v[30:31], v[36:37], v[132:133] op_sel_hi:[1,0]
	v_pk_mul_f32 v[36:37], v[34:35], v[132:133] op_sel_hi:[1,0]
	ds_bpermute_b32 v35, v168, v175
	ds_bpermute_b32 v132, v169, v175
	s_waitcnt lgkmcnt(2)
	v_mul_f32_e32 v34, s40, v176
	s_andn2_b64 vcc, exec, s[6:7]
	s_waitcnt vmcnt(6) lgkmcnt(1)
	v_pk_mul_f32 v[28:29], v[28:29], v[34:35] op_sel_hi:[1,0]
	v_pk_mul_f32 v[26:27], v[26:27], v[34:35] op_sel_hi:[1,0]
	v_mul_f32_e32 v34, s40, v35
	s_waitcnt vmcnt(5)
	v_pk_mul_f32 v[24:25], v[24:25], v[34:35] op_sel_hi:[1,0]
	v_pk_mul_f32 v[22:23], v[22:23], v[34:35] op_sel_hi:[1,0]
	ds_bpermute_b32 v35, v170, v175
	s_waitcnt lgkmcnt(1)
	v_mul_f32_e32 v34, s40, v132
	ds_bpermute_b32 v132, v171, v175
	s_waitcnt vmcnt(4) lgkmcnt(1)
	v_pk_mul_f32 v[16:17], v[16:17], v[34:35] op_sel_hi:[1,0]
	v_pk_mul_f32 v[14:15], v[14:15], v[34:35] op_sel_hi:[1,0]
	v_mul_f32_e32 v34, s40, v35
	s_waitcnt vmcnt(3)
	v_pk_mul_f32 v[8:9], v[8:9], v[34:35] op_sel_hi:[1,0]
	v_pk_mul_f32 v[6:7], v[6:7], v[34:35] op_sel_hi:[1,0]
	ds_bpermute_b32 v35, v172, v175
	s_waitcnt lgkmcnt(1)
	v_mul_f32_e32 v34, s40, v132
	ds_bpermute_b32 v132, v173, v175
	s_waitcnt vmcnt(2) lgkmcnt(1)
	v_pk_mul_f32 v[4:5], v[4:5], v[34:35] op_sel_hi:[1,0]
	v_pk_mul_f32 v[2:3], v[2:3], v[34:35] op_sel_hi:[1,0]
	v_mul_f32_e32 v34, s40, v35
	s_waitcnt vmcnt(1)
	v_pk_mul_f32 v[178:179], v[18:19], v[34:35] op_sel_hi:[1,0]
	s_waitcnt lgkmcnt(0)
	v_mul_f32_e32 v18, s40, v132
	s_waitcnt vmcnt(0)
	v_pk_mul_f32 v[180:181], v[12:13], v[18:19] op_sel_hi:[1,0]
	v_pk_mul_f32 v[182:183], v[10:11], v[18:19] op_sel_hi:[1,0]
	v_mov_b32_e32 v10, v133
	v_mov_b32_e32 v11, v133
	v_mov_b32_e32 v12, v133
	v_mov_b32_e32 v13, v133
	v_cvt_pk_fp8_f32 v10, v126, v136
	v_cvt_pk_fp8_f32 v11, v114, v116
	v_cvt_pk_fp8_f32 v12, v98, v100
	v_cvt_pk_fp8_f32 v13, v82, v84
	v_cvt_pk_fp8_f32 v10, v122, v124 op_sel:[0,0,1]
	v_cvt_pk_fp8_f32 v11, v106, v108 op_sel:[0,0,1]
	v_cvt_pk_fp8_f32 v12, v90, v92 op_sel:[0,0,1]
	v_cvt_pk_fp8_f32 v13, v74, v76 op_sel:[0,0,1]
	v_bitop3_b32 v19, s4, v138, v139 bitop3:0x36
	v_lshl_add_u32 v74, v19, 4, v174
	v_or_b32_e32 v18, s4, v139
	ds_write_b128 v74, v[10:13]
	v_mov_b32_e32 v10, v133
	v_mov_b32_e32 v11, v133
	v_mov_b32_e32 v12, v133
	v_mov_b32_e32 v13, v133
	v_pk_mul_f32 v[176:177], v[20:21], v[34:35] op_sel_hi:[1,0]
	v_cvt_pk_fp8_f32 v10, v66, v68
	v_cvt_pk_fp8_f32 v11, v50, v52
	v_cvt_pk_fp8_f32 v12, v36, v26
	v_cvt_pk_fp8_f32 v13, v6, v2
	v_bitop3_b32 v2, v18, v138, 1 bitop3:0x36
	v_mov_b32_e32 v18, v133
	v_mov_b32_e32 v19, v133
	v_mov_b32_e32 v20, v133
	v_mov_b32_e32 v21, v133
	v_mov_b32_e32 v36, v133
	v_cvt_pk_fp8_f32 v18, v127, v137
	v_cvt_pk_fp8_f32 v19, v115, v117
	v_cvt_pk_fp8_f32 v20, v99, v101
	v_cvt_pk_fp8_f32 v21, v83, v85
	v_mov_b32_e32 v34, v133
	v_mov_b32_e32 v35, v133
	v_cvt_pk_fp8_f32 v36, v37, v27
	v_mov_b32_e32 v37, v133
	v_cvt_pk_fp8_f32 v34, v67, v69
	v_cvt_pk_fp8_f32 v35, v51, v53
	v_cvt_pk_fp8_f32 v37, v7, v3
	v_cvt_pk_fp8_f32 v10, v58, v60 op_sel:[0,0,1]
	v_cvt_pk_fp8_f32 v11, v42, v44 op_sel:[0,0,1]
	v_cvt_pk_fp8_f32 v12, v22, v14 op_sel:[0,0,1]
	v_cvt_pk_fp8_f32 v13, v178, v182 op_sel:[0,0,1]
	v_cvt_pk_fp8_f32 v18, v123, v125 op_sel:[0,0,1]
	v_cvt_pk_fp8_f32 v19, v107, v109 op_sel:[0,0,1]
	v_cvt_pk_fp8_f32 v20, v91, v93 op_sel:[0,0,1]
	v_cvt_pk_fp8_f32 v21, v75, v77 op_sel:[0,0,1]
	v_cvt_pk_fp8_f32 v34, v59, v61 op_sel:[0,0,1]
	v_cvt_pk_fp8_f32 v35, v43, v45 op_sel:[0,0,1]
	v_cvt_pk_fp8_f32 v36, v23, v15 op_sel:[0,0,1]
	v_cvt_pk_fp8_f32 v37, v179, v183 op_sel:[0,0,1]
	v_lshl_add_u32 v2, v2, 4, v174
	ds_write_b128 v2, v[10:13]
	ds_write_b128 v74, v[18:21] offset:128
	ds_write_b128 v2, v[34:37] offset:128
	v_mov_b32_e32 v10, v133
	v_mov_b32_e32 v11, v133
	v_mov_b32_e32 v12, v133
	v_mov_b32_e32 v13, v133
	v_cvt_pk_fp8_f32 v10, v128, v120
	v_cvt_pk_fp8_f32 v11, v110, v104
	v_cvt_pk_fp8_f32 v12, v94, v88
	v_cvt_pk_fp8_f32 v13, v78, v72
	v_mov_b32_e32 v18, v133
	v_mov_b32_e32 v19, v133
	v_mov_b32_e32 v20, v133
	v_mov_b32_e32 v21, v133
	v_cvt_pk_fp8_f32 v18, v62, v56
	v_cvt_pk_fp8_f32 v19, v46, v40
	v_cvt_pk_fp8_f32 v20, v30, v28
	v_cvt_pk_fp8_f32 v21, v8, v4
	v_mov_b32_e32 v34, v133
	v_mov_b32_e32 v35, v133
	v_mov_b32_e32 v36, v133
	v_mov_b32_e32 v37, v133
	v_mov_b32_e32 v28, v133
	v_cvt_pk_fp8_f32 v34, v129, v121
	v_cvt_pk_fp8_f32 v35, v111, v105
	v_cvt_pk_fp8_f32 v36, v95, v89
	v_cvt_pk_fp8_f32 v37, v79, v73
	v_mov_b32_e32 v26, v133
	v_mov_b32_e32 v27, v133
	v_cvt_pk_fp8_f32 v28, v31, v29
	v_mov_b32_e32 v29, v133
	v_cvt_pk_fp8_f32 v26, v63, v57
	v_cvt_pk_fp8_f32 v27, v47, v41
	v_cvt_pk_fp8_f32 v29, v9, v5
	v_cvt_pk_fp8_f32 v10, v118, v112 op_sel:[0,0,1]
	v_cvt_pk_fp8_f32 v11, v102, v96 op_sel:[0,0,1]
	v_cvt_pk_fp8_f32 v12, v86, v80 op_sel:[0,0,1]
	v_cvt_pk_fp8_f32 v13, v70, v64 op_sel:[0,0,1]
	v_cvt_pk_fp8_f32 v18, v54, v48 op_sel:[0,0,1]
	v_cvt_pk_fp8_f32 v19, v38, v32 op_sel:[0,0,1]
	v_cvt_pk_fp8_f32 v20, v24, v16 op_sel:[0,0,1]
	v_cvt_pk_fp8_f32 v21, v176, v180 op_sel:[0,0,1]
	v_cvt_pk_fp8_f32 v34, v119, v113 op_sel:[0,0,1]
	v_cvt_pk_fp8_f32 v35, v103, v97 op_sel:[0,0,1]
	v_cvt_pk_fp8_f32 v36, v87, v81 op_sel:[0,0,1]
	v_cvt_pk_fp8_f32 v37, v71, v65 op_sel:[0,0,1]
	s_mov_b32 s4, 1
	v_cvt_pk_fp8_f32 v26, v55, v49 op_sel:[0,0,1]
	v_cvt_pk_fp8_f32 v27, v39, v33 op_sel:[0,0,1]
	v_cvt_pk_fp8_f32 v28, v25, v17 op_sel:[0,0,1]
	v_cvt_pk_fp8_f32 v29, v177, v181 op_sel:[0,0,1]
	ds_write_b128 v74, v[10:13] offset:256
	ds_write_b128 v2, v[18:21] offset:256
	ds_write_b128 v74, v[34:37] offset:384
	ds_write_b128 v2, v[26:29] offset:384
	s_cbranch_vccz .LBB0_43

.LBB0_79:
	v_lshl_or_b32 v86, s19, 18, v175
	s_lshl_b32 s20, s19, 2
	v_lshl_add_u64 v[84:85], v[34:35], 0, v[86:87]
	v_or_b32_e32 v41, s20, v139
	v_bitop3_b32 v42, s20, v140, v139 bitop3:0x36
	v_add_co_u32_e32 v40, vcc, 0x1000, v84
	v_lshl_add_u32 v86, v42, 4, v174
	v_bitop3_b32 v42, v41, v140, 1 bitop3:0x36
	s_nop 1
	v_addc_co_u32_e32 v41, vcc, 0, v85, vcc
	v_add_co_u32_e32 v44, vcc, 0x2000, v84
	global_load_dwordx4 v[36:39], v[84:85], off nt
	s_nop 1
	v_addc_co_u32_e32 v45, vcc, 0, v85, vcc
	v_add_co_u32_e32 v48, vcc, 0x3000, v84
	v_lshl_add_u32 v89, v42, 4, v174
	s_nop 1
	v_addc_co_u32_e32 v49, vcc, 0, v85, vcc
	v_add_co_u32_e32 v52, vcc, 0x4000, v84
	global_load_dwordx4 v[40:43], v[40:41], off nt
	s_nop 1
	v_addc_co_u32_e32 v53, vcc, 0, v85, vcc
	v_add_co_u32_e32 v56, vcc, 0x5000, v84
	global_load_dwordx4 v[44:47], v[44:45], off nt
	s_nop 1
	global_load_dwordx4 v[48:51], v[48:49], off nt
	s_nop 1
	v_addc_co_u32_e32 v57, vcc, 0, v85, vcc
	v_add_co_u32_e32 v60, vcc, 0x6000, v84
	global_load_dwordx4 v[52:55], v[52:53], off nt
	s_nop 1
	global_load_dwordx4 v[56:59], v[56:57], off nt
	s_nop 1
	v_addc_co_u32_e32 v61, vcc, 0, v85, vcc
	v_add_co_u32_e32 v64, vcc, 0x7000, v84
	s_nop 1
	v_addc_co_u32_e32 v65, vcc, 0, v85, vcc
	v_add_co_u32_e32 v68, vcc, 0x8000, v84
	global_load_dwordx4 v[60:63], v[60:61], off nt
	s_nop 1
	global_load_dwordx4 v[64:67], v[64:65], off nt
	s_nop 1
	v_addc_co_u32_e32 v69, vcc, 0, v85, vcc
	v_add_co_u32_e32 v72, vcc, 0x9000, v84
	s_nop 1
	v_addc_co_u32_e32 v73, vcc, 0, v85, vcc
	v_add_co_u32_e32 v76, vcc, 0xa000, v84
	global_load_dwordx4 v[68:71], v[68:69], off nt
	s_nop 1
	global_load_dwordx4 v[72:75], v[72:73], off nt
	s_nop 1
	v_addc_co_u32_e32 v77, vcc, 0, v85, vcc
	v_add_co_u32_e32 v80, vcc, 0xb000, v84
	s_nop 1
	v_addc_co_u32_e32 v81, vcc, 0, v85, vcc
	v_add_co_u32_e32 v90, vcc, 0xc000, v84
	global_load_dwordx4 v[76:79], v[76:77], off nt
	s_nop 1
	global_load_dwordx4 v[80:83], v[80:81], off nt
	s_nop 1
	v_addc_co_u32_e32 v91, vcc, 0, v85, vcc
	v_add_co_u32_e32 v94, vcc, 0xd000, v84
	s_nop 1
	v_addc_co_u32_e32 v95, vcc, 0, v85, vcc
	v_add_co_u32_e32 v98, vcc, 0xe000, v84
	global_load_dwordx4 v[90:93], v[90:91], off nt
	s_nop 1
	global_load_dwordx4 v[94:97], v[94:95], off nt
	s_nop 1
	v_addc_co_u32_e32 v99, vcc, 0, v85, vcc
	v_add_co_u32_e32 v102, vcc, 0xf000, v84
	s_nop 1
	v_addc_co_u32_e32 v103, vcc, 0, v85, vcc
	v_add_co_u32_e32 v106, vcc, 0x10000, v84
	global_load_dwordx4 v[98:101], v[98:99], off nt
	s_nop 1
	global_load_dwordx4 v[102:105], v[102:103], off nt
	s_nop 1
	v_addc_co_u32_e32 v107, vcc, 0, v85, vcc
	v_add_co_u32_e32 v110, vcc, 0x11000, v84
	s_nop 1
	v_addc_co_u32_e32 v111, vcc, 0, v85, vcc
	v_add_co_u32_e32 v114, vcc, 0x12000, v84
	global_load_dwordx4 v[106:109], v[106:107], off nt
	s_nop 1
	global_load_dwordx4 v[110:113], v[110:111], off nt
	s_nop 1
	v_addc_co_u32_e32 v115, vcc, 0, v85, vcc
	v_add_co_u32_e32 v118, vcc, 0x13000, v84
	s_nop 1
	v_addc_co_u32_e32 v119, vcc, 0, v85, vcc
	v_add_co_u32_e32 v122, vcc, 0x14000, v84
	global_load_dwordx4 v[114:117], v[114:115], off nt
	s_nop 1
	global_load_dwordx4 v[118:121], v[118:119], off nt
	s_nop 1
	v_addc_co_u32_e32 v123, vcc, 0, v85, vcc
	v_add_co_u32_e32 v126, vcc, 0x15000, v84
	s_nop 1
	v_addc_co_u32_e32 v127, vcc, 0, v85, vcc
	v_add_co_u32_e32 v130, vcc, 0x16000, v84
	global_load_dwordx4 v[122:125], v[122:123], off nt
	s_nop 1
	global_load_dwordx4 v[126:129], v[126:127], off nt
	s_nop 1
	v_addc_co_u32_e32 v131, vcc, 0, v85, vcc
	v_add_co_u32_e32 v134, vcc, 0x17000, v84
	s_nop 1
	v_addc_co_u32_e32 v135, vcc, 0, v85, vcc
	v_add_co_u32_e32 v178, vcc, 0x18000, v84
	global_load_dwordx4 v[130:133], v[130:131], off nt
	s_nop 1
	global_load_dwordx4 v[134:137], v[134:135], off nt
	s_nop 1
	v_addc_co_u32_e32 v179, vcc, 0, v85, vcc
	v_add_co_u32_e32 v182, vcc, 0x19000, v84
	s_nop 1
	v_addc_co_u32_e32 v183, vcc, 0, v85, vcc
	v_add_co_u32_e32 v186, vcc, 0x1a000, v84
	global_load_dwordx4 v[178:181], v[178:179], off nt
	s_nop 1
	global_load_dwordx4 v[182:185], v[182:183], off nt
	s_nop 1
	v_addc_co_u32_e32 v187, vcc, 0, v85, vcc
	v_add_co_u32_e32 v190, vcc, 0x1b000, v84
	s_nop 1
	v_addc_co_u32_e32 v191, vcc, 0, v85, vcc
	v_add_co_u32_e32 v194, vcc, 0x1c000, v84
	global_load_dwordx4 v[186:189], v[186:187], off nt
	s_nop 1
	global_load_dwordx4 v[190:193], v[190:191], off nt
	s_nop 1
	v_addc_co_u32_e32 v195, vcc, 0, v85, vcc
	v_add_co_u32_e32 v198, vcc, 0x1d000, v84
	s_nop 1
	v_addc_co_u32_e32 v199, vcc, 0, v85, vcc
	global_load_dwordx4 v[194:197], v[194:195], off nt
	s_nop 1
	global_load_dwordx4 v[198:201], v[198:199], off nt
	v_add_co_u32_e32 v202, vcc, 0x1e000, v84
	s_nop 1
	v_addc_co_u32_e32 v203, vcc, 0, v85, vcc
	v_add_co_u32_e32 v84, vcc, 0x1f000, v84
	s_nop 1
	v_addc_co_u32_e32 v85, vcc, 0, v85, vcc
	global_load_dwordx4 v[202:205], v[202:203], off nt
	s_nop 1
	global_load_dwordx4 v[206:209], v[84:85], off nt
	s_nop 1
	s_nop 0
	s_nop 0
	s_nop 0
	s_nop 0
	s_nop 0
	s_nop 1
	v_mov_b32_e32 v6, v87
	s_nop 0
	s_nop 0
	s_nop 1
	v_mov_b32_e32 v14, v87
	s_nop 0
	s_nop 0
	s_nop 1
	v_mov_b32_e32 v22, v87
	s_nop 0
	s_nop 0
	s_nop 1
	v_mov_b32_e32 v30, v87
	s_nop 0
	s_nop 0
	s_nop 1
	v_mov_b32_e32 v7, v87
	s_nop 0
	s_nop 0
	s_nop 1
	v_mov_b32_e32 v15, v87
	s_nop 0
	s_nop 0
	s_waitcnt vmcnt(31)
	v_pk_mul_f32 v[38:39], v[38:39], s[6:7] op_sel_hi:[1,0]
	s_nop 0
	s_nop 1
	v_pk_mul_f32 v[36:37], v[36:37], s[6:7] op_sel_hi:[1,0]
	s_nop 0
	s_nop 0
	s_waitcnt vmcnt(30)
	v_pk_mul_f32 v[42:43], v[42:43], s[6:7] op_sel_hi:[1,0]
	s_nop 0
	s_nop 1
	v_pk_mul_f32 v[40:41], v[40:41], s[6:7] op_sel_hi:[1,0]
	s_nop 0
	s_nop 0
	s_nop 1
	v_cvt_pk_fp8_f32 v6, v36, v40
	s_nop 0
	s_nop 0
	s_nop 1
	v_cvt_pk_fp8_f32 v14, v37, v41
	s_nop 0
	s_nop 0
	s_nop 1
	v_cvt_pk_fp8_f32 v22, v38, v42
	s_nop 0
	s_nop 1
	v_cvt_pk_fp8_f32 v30, v39, v43
	s_nop 0
	s_nop 0
	s_nop 1
	v_mov_b32_e32 v23, v87
	v_mov_b32_e32 v31, v87
	s_waitcnt vmcnt(29)
	v_pk_mul_f32 v[46:47], v[46:47], s[6:7] op_sel_hi:[1,0]
	v_pk_mul_f32 v[44:45], v[44:45], s[6:7] op_sel_hi:[1,0]
	s_waitcnt vmcnt(28)
	v_pk_mul_f32 v[36:37], v[50:51], s[6:7] op_sel_hi:[1,0]
	v_pk_mul_f32 v[38:39], v[48:49], s[6:7] op_sel_hi:[1,0]
	s_waitcnt vmcnt(27)
	v_pk_mul_f32 v[40:41], v[54:55], s[6:7] op_sel_hi:[1,0]
	v_pk_mul_f32 v[42:43], v[52:53], s[6:7] op_sel_hi:[1,0]
	s_waitcnt vmcnt(26)
	v_pk_mul_f32 v[48:49], v[58:59], s[6:7] op_sel_hi:[1,0]
	v_pk_mul_f32 v[50:51], v[56:57], s[6:7] op_sel_hi:[1,0]
	v_mov_b32_e32 v8, v87
	v_mov_b32_e32 v16, v87
	v_mov_b32_e32 v24, v87
	v_mov_b32_e32 v32, v87
	v_cvt_pk_fp8_f32 v6, v44, v38 op_sel:[0,0,1]
	v_cvt_pk_fp8_f32 v7, v42, v50
	v_cvt_pk_fp8_f32 v14, v45, v39 op_sel:[0,0,1]
	v_cvt_pk_fp8_f32 v15, v43, v51
	v_cvt_pk_fp8_f32 v22, v46, v36 op_sel:[0,0,1]
	v_cvt_pk_fp8_f32 v23, v40, v48
	v_cvt_pk_fp8_f32 v30, v47, v37 op_sel:[0,0,1]
	v_cvt_pk_fp8_f32 v31, v41, v49
	s_waitcnt vmcnt(23)
	v_pk_mul_f32 v[40:41], v[70:71], s[6:7] op_sel_hi:[1,0]
	v_pk_mul_f32 v[42:43], v[68:69], s[6:7] op_sel_hi:[1,0]
	s_waitcnt vmcnt(22)
	v_pk_mul_f32 v[44:45], v[74:75], s[6:7] op_sel_hi:[1,0]
	v_pk_mul_f32 v[46:47], v[72:73], s[6:7] op_sel_hi:[1,0]
	v_mov_b32_e32 v17, v87
	v_mov_b32_e32 v25, v87
	v_cvt_pk_fp8_f32 v8, v42, v46
	v_cvt_pk_fp8_f32 v16, v43, v47
	v_cvt_pk_fp8_f32 v24, v40, v44
	v_cvt_pk_fp8_f32 v32, v41, v45
	s_waitcnt vmcnt(19)
	v_pk_mul_f32 v[40:41], v[92:93], s[6:7] op_sel_hi:[1,0]
	v_pk_mul_f32 v[42:43], v[90:91], s[6:7] op_sel_hi:[1,0]
	s_waitcnt vmcnt(18)
	v_pk_mul_f32 v[44:45], v[96:97], s[6:7] op_sel_hi:[1,0]
	v_pk_mul_f32 v[46:47], v[94:95], s[6:7] op_sel_hi:[1,0]
	v_cvt_pk_fp8_f32 v25, v40, v44
	v_cvt_pk_fp8_f32 v17, v43, v47
	v_pk_mul_f32 v[52:53], v[62:63], s[6:7] op_sel_hi:[1,0]
	v_pk_mul_f32 v[54:55], v[60:61], s[6:7] op_sel_hi:[1,0]
	v_pk_mul_f32 v[36:37], v[66:67], s[6:7] op_sel_hi:[1,0]
	v_pk_mul_f32 v[38:39], v[64:65], s[6:7] op_sel_hi:[1,0]
	v_mov_b32_e32 v9, v87
	v_pk_mul_f32 v[48:49], v[78:79], s[6:7] op_sel_hi:[1,0]
	v_pk_mul_f32 v[50:51], v[76:77], s[6:7] op_sel_hi:[1,0]
	v_cvt_pk_fp8_f32 v7, v54, v38 op_sel:[0,0,1]
	v_cvt_pk_fp8_f32 v15, v55, v39 op_sel:[0,0,1]
	v_cvt_pk_fp8_f32 v23, v52, v36 op_sel:[0,0,1]
	v_cvt_pk_fp8_f32 v31, v53, v37 op_sel:[0,0,1]
	v_pk_mul_f32 v[36:37], v[82:83], s[6:7] op_sel_hi:[1,0]
	v_pk_mul_f32 v[38:39], v[80:81], s[6:7] op_sel_hi:[1,0]
	v_mov_b32_e32 v33, v87
	s_waitcnt vmcnt(17)
	v_pk_mul_f32 v[52:53], v[100:101], s[6:7] op_sel_hi:[1,0]
	v_pk_mul_f32 v[54:55], v[98:99], s[6:7] op_sel_hi:[1,0]
	v_cvt_pk_fp8_f32 v8, v50, v38 op_sel:[0,0,1]
	v_cvt_pk_fp8_f32 v9, v42, v46
	v_cvt_pk_fp8_f32 v16, v51, v39 op_sel:[0,0,1]
	v_cvt_pk_fp8_f32 v24, v48, v36 op_sel:[0,0,1]
	v_cvt_pk_fp8_f32 v32, v49, v37 op_sel:[0,0,1]
	s_waitcnt vmcnt(16)
	v_pk_mul_f32 v[36:37], v[104:105], s[6:7] op_sel_hi:[1,0]
	v_pk_mul_f32 v[38:39], v[102:103], s[6:7] op_sel_hi:[1,0]
	v_cvt_pk_fp8_f32 v33, v41, v45
	v_cvt_pk_fp8_f32 v17, v55, v39 op_sel:[0,0,1]
	v_cvt_pk_fp8_f32 v25, v52, v36 op_sel:[0,0,1]
	v_mov_b32_e32 v2, v87
	v_mov_b32_e32 v10, v87
	s_waitcnt vmcnt(15)
	v_pk_mul_f32 v[42:43], v[106:107], s[6:7] op_sel_hi:[1,0]
	s_waitcnt vmcnt(14)
	v_pk_mul_f32 v[46:47], v[110:111], s[6:7] op_sel_hi:[1,0]
	v_mov_b32_e32 v3, v87
	v_mov_b32_e32 v11, v87
	v_cvt_pk_fp8_f32 v9, v54, v38 op_sel:[0,0,1]
	v_cvt_pk_fp8_f32 v2, v42, v46
	v_cvt_pk_fp8_f32 v10, v43, v47
	s_waitcnt vmcnt(11)
	v_pk_mul_f32 v[42:43], v[122:123], s[6:7] op_sel_hi:[1,0]
	s_waitcnt vmcnt(10)
	v_pk_mul_f32 v[46:47], v[126:127], s[6:7] op_sel_hi:[1,0]
	v_mov_b32_e32 v4, v87
	v_mov_b32_e32 v12, v87
	v_mov_b32_e32 v18, v87
	v_mov_b32_e32 v26, v87
	v_pk_mul_f32 v[40:41], v[108:109], s[6:7] op_sel_hi:[1,0]
	v_pk_mul_f32 v[44:45], v[112:113], s[6:7] op_sel_hi:[1,0]
	v_cvt_pk_fp8_f32 v33, v53, v37 op_sel:[0,0,1]
	v_cvt_pk_fp8_f32 v3, v42, v46
	ds_write_b128 v86, v[14:17] offset:128
	v_cvt_pk_fp8_f32 v11, v43, v47
	ds_write_b128 v86, v[22:25] offset:256
	s_waitcnt vmcnt(7)
	v_pk_mul_f32 v[16:17], v[178:179], s[6:7] op_sel_hi:[1,0]
	s_waitcnt vmcnt(6)
	v_pk_mul_f32 v[24:25], v[182:183], s[6:7] op_sel_hi:[1,0]
	v_mov_b32_e32 v5, v87
	v_mov_b32_e32 v19, v87
	v_mov_b32_e32 v27, v87
	v_cvt_pk_fp8_f32 v18, v40, v44
	v_cvt_pk_fp8_f32 v26, v41, v45
	v_pk_mul_f32 v[40:41], v[124:125], s[6:7] op_sel_hi:[1,0]
	v_pk_mul_f32 v[44:45], v[128:129], s[6:7] op_sel_hi:[1,0]
	v_cvt_pk_fp8_f32 v4, v16, v24
	v_cvt_pk_fp8_f32 v12, v17, v25
	s_waitcnt vmcnt(3)
	v_pk_mul_f32 v[16:17], v[194:195], s[6:7] op_sel_hi:[1,0]
	s_waitcnt vmcnt(2)
	v_pk_mul_f32 v[24:25], v[198:199], s[6:7] op_sel_hi:[1,0]
	v_mov_b32_e32 v13, v87
	v_mov_b32_e32 v20, v87
	v_mov_b32_e32 v28, v87
	v_cvt_pk_fp8_f32 v19, v40, v44
	v_cvt_pk_fp8_f32 v27, v41, v45
	v_pk_mul_f32 v[14:15], v[180:181], s[6:7] op_sel_hi:[1,0]
	v_pk_mul_f32 v[22:23], v[184:185], s[6:7] op_sel_hi:[1,0]
	v_cvt_pk_fp8_f32 v5, v16, v24
	v_mov_b32_e32 v21, v87
	v_pk_mul_f32 v[54:55], v[130:131], s[6:7] op_sel_hi:[1,0]
	ds_write_b128 v86, v[6:9]
	v_pk_mul_f32 v[8:9], v[134:135], s[6:7] op_sel_hi:[1,0]
	v_cvt_pk_fp8_f32 v20, v14, v22
	v_cvt_pk_fp8_f32 v28, v15, v23
	v_pk_mul_f32 v[14:15], v[196:197], s[6:7] op_sel_hi:[1,0]
	v_pk_mul_f32 v[22:23], v[200:201], s[6:7] op_sel_hi:[1,0]
	v_cvt_pk_fp8_f32 v13, v17, v25
	v_mov_b32_e32 v29, v87
	v_pk_mul_f32 v[50:51], v[114:115], s[6:7] op_sel_hi:[1,0]
	v_pk_mul_f32 v[38:39], v[118:119], s[6:7] op_sel_hi:[1,0]
	ds_write_b128 v86, v[30:33] offset:384
	v_pk_mul_f32 v[32:33], v[186:187], s[6:7] op_sel_hi:[1,0]
	v_cvt_pk_fp8_f32 v3, v54, v8 op_sel:[0,0,1]
	v_cvt_pk_fp8_f32 v11, v55, v9 op_sel:[0,0,1]
	v_pk_mul_f32 v[8:9], v[190:191], s[6:7] op_sel_hi:[1,0]
	v_cvt_pk_fp8_f32 v21, v14, v22
	v_pk_mul_f32 v[52:53], v[132:133], s[6:7] op_sel_hi:[1,0]
	v_cvt_pk_fp8_f32 v2, v50, v38 op_sel:[0,0,1]
	v_cvt_pk_fp8_f32 v10, v51, v39 op_sel:[0,0,1]
	v_pk_mul_f32 v[6:7], v[136:137], s[6:7] op_sel_hi:[1,0]
	s_waitcnt vmcnt(1)
	v_pk_mul_f32 v[38:39], v[202:203], s[6:7] op_sel_hi:[1,0]
	v_cvt_pk_fp8_f32 v4, v32, v8 op_sel:[0,0,1]
	v_cvt_pk_fp8_f32 v12, v33, v9 op_sel:[0,0,1]
	v_cvt_pk_fp8_f32 v29, v15, v23
	s_waitcnt vmcnt(0)
	v_pk_mul_f32 v[8:9], v[206:207], s[6:7] op_sel_hi:[1,0]
	v_pk_mul_f32 v[48:49], v[116:117], s[6:7] op_sel_hi:[1,0]
	v_pk_mul_f32 v[36:37], v[120:121], s[6:7] op_sel_hi:[1,0]
	v_pk_mul_f32 v[30:31], v[188:189], s[6:7] op_sel_hi:[1,0]
	v_cvt_pk_fp8_f32 v19, v52, v6 op_sel:[0,0,1]
	v_cvt_pk_fp8_f32 v27, v53, v7 op_sel:[0,0,1]
	v_pk_mul_f32 v[6:7], v[192:193], s[6:7] op_sel_hi:[1,0]
	v_cvt_pk_fp8_f32 v5, v38, v8 op_sel:[0,0,1]
	v_cvt_pk_fp8_f32 v18, v48, v36 op_sel:[0,0,1]
	v_cvt_pk_fp8_f32 v26, v49, v37 op_sel:[0,0,1]
	v_pk_mul_f32 v[36:37], v[204:205], s[6:7] op_sel_hi:[1,0]
	v_cvt_pk_fp8_f32 v20, v30, v6 op_sel:[0,0,1]
	v_cvt_pk_fp8_f32 v28, v31, v7 op_sel:[0,0,1]
	v_pk_mul_f32 v[6:7], v[208:209], s[6:7] op_sel_hi:[1,0]
	v_cvt_pk_fp8_f32 v13, v39, v9 op_sel:[0,0,1]
	s_and_b64 s[0:1], exec, s[12:13]
	v_cvt_pk_fp8_f32 v21, v36, v6 op_sel:[0,0,1]
	s_mov_b32 s19, 1
	s_mov_b64 s[12:13], 0
	v_cvt_pk_fp8_f32 v29, v37, v7 op_sel:[0,0,1]
	s_mov_b64 vcc, s[0:1]
	ds_write_b128 v89, v[2:5]
	ds_write_b128 v89, v[10:13] offset:128
	ds_write_b128 v89, v[18:21] offset:256
	ds_write_b128 v89, v[26:29] offset:384
	s_cbranch_vccnz .LBB0_79
	s_lshl_b32 s0, s15, 10
	s_or_b32 s0, s0, s17
	s_mulk_i32 s0, 0xb00
	s_add_u32 s0, s25, s0
	s_addc_u32 s1, s26, 0
	s_waitcnt lgkmcnt(0)
	v_mov_b32_e32 v14, v166
	s_add_u32 s0, s0, s14
	s_addc_u32 s1, s1, s16
	v_lshlrev_b32_e32 v2, 4, v14
	v_and_b32_e32 v86, 0x70, v2
	v_ashrrev_i32_e32 v15, 3, v14
	v_lshl_add_u64 v[2:3], s[0:1], 0, v[86:87]
	v_lshl_add_u64 v[10:11], v[2:3], 0, s[8:9]
	v_lshrrev_b32_e32 v3, 2, v15
	v_add_u32_e32 v17, 8, v15
	v_xor_b32_e32 v3, v3, v14
	v_lshrrev_b32_e32 v7, 2, v17
	v_lshlrev_b32_e32 v3, 4, v3
	v_xor_b32_e32 v7, v7, v14
	v_lshlrev_b32_e32 v2, 7, v15
	v_and_b32_e32 v16, 0x70, v3
	v_lshlrev_b32_e32 v7, 4, v7
	v_add3_u32 v2, s29, v2, v16
	v_lshlrev_b32_e32 v6, 7, v17
	v_and_b32_e32 v7, 0x70, v7
	ds_read_b128 v[2:5], v2
	v_add3_u32 v6, s29, v6, v7
	ds_read_b128 v[6:9], v6
	v_mad_i64_i32 v[12:13], s[0:1], v15, s24, v[10:11]
	s_waitcnt lgkmcnt(1)
	global_store_dwordx4 v[12:13], v[2:5], off nt
	v_add_u32_e32 v12, 16, v15
	s_nop 0
	v_mad_i64_i32 v[2:3], s[0:1], v17, s24, v[10:11]
	s_waitcnt lgkmcnt(0)
	global_store_dwordx4 v[2:3], v[6:9], off nt
	v_lshrrev_b32_e32 v3, 2, v12
	v_add_u32_e32 v17, 24, v15
	v_xor_b32_e32 v3, v3, v14
	v_lshrrev_b32_e32 v7, 2, v17
	v_lshlrev_b32_e32 v3, 4, v3
	v_xor_b32_e32 v7, v7, v14
	v_lshlrev_b32_e32 v2, 7, v12
	v_and_b32_e32 v3, 0x70, v3
	v_lshlrev_b32_e32 v7, 4, v7
	v_add3_u32 v2, s29, v2, v3
	v_lshlrev_b32_e32 v6, 7, v17
	v_and_b32_e32 v7, 0x70, v7
	ds_read_b128 v[2:5], v2
	v_add3_u32 v6, s29, v6, v7
	ds_read_b128 v[6:9], v6
	v_mad_i64_i32 v[12:13], s[0:1], v12, s24, v[10:11]
	s_waitcnt lgkmcnt(1)
	global_store_dwordx4 v[12:13], v[2:5], off nt
	v_add_u32_e32 v12, 32, v15
	s_nop 0
	v_mad_i64_i32 v[2:3], s[0:1], v17, s24, v[10:11]
	v_add_u32_e32 v17, 40, v15
	s_waitcnt lgkmcnt(0)
	global_store_dwordx4 v[2:3], v[6:9], off nt
	v_lshlrev_b32_e32 v2, 7, v12
	v_add3_u32 v2, s29, v2, v16
	v_lshrrev_b32_e32 v7, 2, v17
	v_xor_b32_e32 v7, v7, v14
	v_lshlrev_b32_e32 v7, 4, v7
	v_lshlrev_b32_e32 v6, 7, v17
	v_and_b32_e32 v7, 0x70, v7
	ds_read_b128 v[2:5], v2
	v_add3_u32 v6, s29, v6, v7
	ds_read_b128 v[6:9], v6
	v_mad_i64_i32 v[12:13], s[0:1], v12, s24, v[10:11]
	s_waitcnt lgkmcnt(1)
	global_store_dwordx4 v[12:13], v[2:5], off nt
	v_add_u32_e32 v12, 48, v15
	s_nop 0
	v_mad_i64_i32 v[2:3], s[0:1], v17, s24, v[10:11]
	s_waitcnt lgkmcnt(0)
	global_store_dwordx4 v[2:3], v[6:9], off nt
	v_lshrrev_b32_e32 v3, 2, v12
	v_add_u32_e32 v17, 56, v15
	v_xor_b32_e32 v3, v3, v14
	v_lshrrev_b32_e32 v7, 2, v17
	v_lshlrev_b32_e32 v3, 4, v3
	v_xor_b32_e32 v7, v7, v14
	v_lshlrev_b32_e32 v2, 7, v12
	v_and_b32_e32 v3, 0x70, v3
	v_lshlrev_b32_e32 v7, 4, v7
	v_add3_u32 v2, s29, v2, v3
	v_lshlrev_b32_e32 v6, 7, v17
	v_and_b32_e32 v7, 0x70, v7
	ds_read_b128 v[2:5], v2
	v_add3_u32 v6, s29, v6, v7
	ds_read_b128 v[6:9], v6
	v_mad_i64_i32 v[12:13], s[0:1], v12, s24, v[10:11]
	s_waitcnt lgkmcnt(1)
	global_store_dwordx4 v[12:13], v[2:5], off nt
	v_add_u32_e32 v12, 64, v15
	s_nop 0
	v_mad_i64_i32 v[2:3], s[0:1], v17, s24, v[10:11]
	v_add_u32_e32 v17, 0x48, v15
	s_waitcnt lgkmcnt(0)
	global_store_dwordx4 v[2:3], v[6:9], off nt
	v_lshlrev_b32_e32 v2, 7, v12
	v_add3_u32 v2, s29, v2, v16
	v_lshrrev_b32_e32 v7, 2, v17
	v_xor_b32_e32 v7, v7, v14
	v_lshlrev_b32_e32 v7, 4, v7
	v_lshlrev_b32_e32 v6, 7, v17
	v_and_b32_e32 v7, 0x70, v7
	ds_read_b128 v[2:5], v2
	v_add3_u32 v6, s29, v6, v7
	ds_read_b128 v[6:9], v6
	v_mad_i64_i32 v[12:13], s[0:1], v12, s24, v[10:11]
	s_waitcnt lgkmcnt(1)
	global_store_dwordx4 v[12:13], v[2:5], off nt
	v_add_u32_e32 v12, 0x50, v15
	s_nop 0
	v_mad_i64_i32 v[2:3], s[0:1], v17, s24, v[10:11]
	s_waitcnt lgkmcnt(0)
	global_store_dwordx4 v[2:3], v[6:9], off nt
	v_lshrrev_b32_e32 v3, 2, v12
	v_add_u32_e32 v17, 0x58, v15
	v_xor_b32_e32 v3, v3, v14
	v_lshrrev_b32_e32 v7, 2, v17
	v_lshlrev_b32_e32 v3, 4, v3
	v_xor_b32_e32 v7, v7, v14
	v_lshlrev_b32_e32 v2, 7, v12
	v_and_b32_e32 v3, 0x70, v3
	v_lshlrev_b32_e32 v7, 4, v7
	v_add3_u32 v2, s29, v2, v3
	v_lshlrev_b32_e32 v6, 7, v17
	v_and_b32_e32 v7, 0x70, v7
	ds_read_b128 v[2:5], v2
	v_add3_u32 v6, s29, v6, v7
	ds_read_b128 v[6:9], v6
	v_mad_i64_i32 v[12:13], s[0:1], v12, s24, v[10:11]
	s_waitcnt lgkmcnt(1)
	global_store_dwordx4 v[12:13], v[2:5], off nt
	v_add_u32_e32 v12, 0x60, v15
	s_nop 0
	v_mad_i64_i32 v[2:3], s[0:1], v17, s24, v[10:11]
	s_waitcnt lgkmcnt(0)
	global_store_dwordx4 v[2:3], v[6:9], off nt
	v_lshlrev_b32_e32 v2, 7, v12
	v_add3_u32 v2, s29, v2, v16
	v_add_u32_e32 v16, 0x68, v15
	v_lshrrev_b32_e32 v7, 2, v16
	v_xor_b32_e32 v7, v7, v14
	v_lshlrev_b32_e32 v7, 4, v7
	v_lshlrev_b32_e32 v6, 7, v16
	v_and_b32_e32 v7, 0x70, v7
	ds_read_b128 v[2:5], v2
	v_add3_u32 v6, s29, v6, v7
	ds_read_b128 v[6:9], v6
	v_mad_i64_i32 v[12:13], s[0:1], v12, s24, v[10:11]
	s_waitcnt lgkmcnt(1)
	global_store_dwordx4 v[12:13], v[2:5], off nt
	v_add_u32_e32 v12, 0x70, v15
	v_add_u32_e32 v15, 0x78, v15
	v_mad_i64_i32 v[2:3], s[0:1], v16, s24, v[10:11]
	s_waitcnt lgkmcnt(0)
	global_store_dwordx4 v[2:3], v[6:9], off nt
	v_lshrrev_b32_e32 v3, 2, v12
	v_xor_b32_e32 v3, v3, v14
	v_lshrrev_b32_e32 v7, 2, v15
	v_lshlrev_b32_e32 v3, 4, v3
	v_xor_b32_e32 v7, v7, v14
	v_lshlrev_b32_e32 v2, 7, v12
	v_and_b32_e32 v3, 0x70, v3
	v_lshlrev_b32_e32 v7, 4, v7
	v_add3_u32 v2, s29, v2, v3
	v_lshlrev_b32_e32 v6, 7, v15
	v_and_b32_e32 v7, 0x70, v7
	ds_read_b128 v[2:5], v2
	v_add3_u32 v6, s29, v6, v7
	ds_read_b128 v[6:9], v6
	v_mad_i64_i32 v[12:13], s[0:1], v12, s24, v[10:11]
	s_waitcnt lgkmcnt(1)
	global_store_dwordx4 v[12:13], v[2:5], off nt
	s_nop 1
	v_mad_i64_i32 v[2:3], s[0:1], v15, s24, v[10:11]
	s_waitcnt lgkmcnt(0)
	global_store_dwordx4 v[2:3], v[6:9], off nt
	s_waitcnt lgkmcnt(0)
	s_mov_b64 s[0:1], 0

.LBB0_87:
	v_or_b32_e32 v2, s27, v138
	v_mul_u32_u24_e32 v86, 0x2c00, v2
	v_lshl_add_u64 v[6:7], v[90:91], 0, v[86:87]
	v_add_co_u32_e32 v2, vcc, 0x2000, v6
	s_nop 1
	v_addc_co_u32_e32 v3, vcc, 0, v7, vcc
	global_load_dwordx4 v[94:97], v[6:7], off nt
	global_load_dwordx4 v[98:101], v[2:3], off offset:3072 nt
	v_add_co_u32_e32 v2, vcc, 0x5000, v6
	s_nop 1
	v_addc_co_u32_e32 v3, vcc, 0, v7, vcc
	v_add_co_u32_e32 v4, vcc, 0x8000, v6
	s_nop 1
	v_addc_co_u32_e32 v5, vcc, 0, v7, vcc
	global_load_dwordx4 v[102:105], v[2:3], off offset:2048 nt
	global_load_dwordx4 v[106:109], v[4:5], off offset:1024 nt
	v_add_co_u32_e32 v2, vcc, 0xb000, v6
	s_nop 1
	v_addc_co_u32_e32 v3, vcc, 0, v7, vcc
	v_add_co_u32_e32 v4, vcc, 0xd000, v6
	s_nop 1
	v_addc_co_u32_e32 v5, vcc, 0, v7, vcc
	global_load_dwordx4 v[110:113], v[2:3], off nt
	global_load_dwordx4 v[124:127], v[4:5], off offset:3072 nt
	v_add_co_u32_e32 v2, vcc, 0x10000, v6
	s_nop 1
	v_addc_co_u32_e32 v3, vcc, 0, v7, vcc
	v_add_co_u32_e32 v4, vcc, 0x13000, v6
	s_nop 1
	v_addc_co_u32_e32 v5, vcc, 0, v7, vcc
	global_load_dwordx4 v[128:131], v[2:3], off offset:2048 nt
	global_load_dwordx4 v[132:135], v[4:5], off offset:1024 nt
	v_add_co_u32_e32 v2, vcc, 0x16000, v6
	s_nop 1
	v_addc_co_u32_e32 v3, vcc, 0, v7, vcc
	v_add_co_u32_e32 v4, vcc, 0x18000, v6
	s_nop 1
	v_addc_co_u32_e32 v5, vcc, 0, v7, vcc
	global_load_dwordx4 v[178:181], v[2:3], off nt
	global_load_dwordx4 v[182:185], v[4:5], off offset:3072 nt
	v_add_co_u32_e32 v2, vcc, 0x1b000, v6
	s_nop 1
	v_addc_co_u32_e32 v3, vcc, 0, v7, vcc
	v_add_co_u32_e32 v4, vcc, 0x1e000, v6
	s_nop 1
	v_addc_co_u32_e32 v5, vcc, 0, v7, vcc
	global_load_dwordx4 v[186:189], v[2:3], off offset:2048 nt
	global_load_dwordx4 v[78:81], v[4:5], off offset:1024 nt
	v_add_co_u32_e32 v2, vcc, 0x21000, v6
	s_nop 1
	v_addc_co_u32_e32 v3, vcc, 0, v7, vcc
	v_add_co_u32_e32 v4, vcc, 0x23000, v6
	s_nop 1
	v_addc_co_u32_e32 v5, vcc, 0, v7, vcc
	global_load_dwordx4 v[82:85], v[2:3], off nt
	global_load_dwordx4 v[70:73], v[4:5], off offset:3072 nt
	v_add_co_u32_e32 v2, vcc, 0x26000, v6
	s_nop 1
	v_addc_co_u32_e32 v3, vcc, 0, v7, vcc
	v_add_co_u32_e32 v4, vcc, 0x29000, v6
	s_nop 1
	v_addc_co_u32_e32 v5, vcc, 0, v7, vcc
	global_load_dwordx4 v[74:77], v[2:3], off offset:2048 nt
	global_load_dwordx4 v[62:65], v[4:5], off offset:1024 nt
	v_add_co_u32_e32 v2, vcc, 0x2c000, v6
	s_nop 1
	v_addc_co_u32_e32 v3, vcc, 0, v7, vcc
	v_add_co_u32_e32 v4, vcc, 0x2e000, v6
	s_nop 1
	v_addc_co_u32_e32 v5, vcc, 0, v7, vcc
	global_load_dwordx4 v[66:69], v[2:3], off nt
	global_load_dwordx4 v[54:57], v[4:5], off offset:3072 nt
	v_add_co_u32_e32 v2, vcc, 0x31000, v6
	s_nop 1
	v_addc_co_u32_e32 v3, vcc, 0, v7, vcc
	v_add_co_u32_e32 v4, vcc, 0x34000, v6
	s_nop 1
	v_addc_co_u32_e32 v5, vcc, 0, v7, vcc
	global_load_dwordx4 v[58:61], v[2:3], off offset:2048 nt
	global_load_dwordx4 v[46:49], v[4:5], off offset:1024 nt
	v_add_co_u32_e32 v2, vcc, 0x37000, v6
	s_nop 1
	v_addc_co_u32_e32 v3, vcc, 0, v7, vcc
	v_add_co_u32_e32 v4, vcc, 0x39000, v6
	s_nop 1
	v_addc_co_u32_e32 v5, vcc, 0, v7, vcc
	global_load_dwordx4 v[50:53], v[2:3], off nt
	global_load_dwordx4 v[38:41], v[4:5], off offset:3072 nt
	v_add_co_u32_e32 v2, vcc, 0x3c000, v6
	s_nop 1
	v_addc_co_u32_e32 v3, vcc, 0, v7, vcc
	v_add_co_u32_e32 v4, vcc, 0x3f000, v6
	s_nop 1
	v_addc_co_u32_e32 v5, vcc, 0, v7, vcc
	global_load_dwordx4 v[42:45], v[2:3], off offset:2048 nt
	global_load_dwordx4 v[30:33], v[4:5], off offset:1024 nt
	v_add_co_u32_e32 v2, vcc, 0x42000, v6
	s_nop 1
	v_addc_co_u32_e32 v3, vcc, 0, v7, vcc
	v_add_co_u32_e32 v4, vcc, 0x44000, v6
	s_nop 1
	v_addc_co_u32_e32 v5, vcc, 0, v7, vcc
	global_load_dwordx4 v[34:37], v[2:3], off nt
	global_load_dwordx4 v[22:25], v[4:5], off offset:3072 nt
	v_add_co_u32_e32 v2, vcc, 0x47000, v6
	s_nop 1
	v_addc_co_u32_e32 v3, vcc, 0, v7, vcc
	v_add_co_u32_e32 v4, vcc, 0x4a000, v6
	s_nop 1
	v_addc_co_u32_e32 v5, vcc, 0, v7, vcc
	global_load_dwordx4 v[26:29], v[2:3], off offset:2048 nt
	global_load_dwordx4 v[10:13], v[4:5], off offset:1024 nt
	v_add_co_u32_e32 v2, vcc, 0x4d000, v6
	s_nop 1
	v_addc_co_u32_e32 v3, vcc, 0, v7, vcc
	v_add_co_u32_e32 v4, vcc, 0x4f000, v6
	s_nop 1
	v_addc_co_u32_e32 v5, vcc, 0, v7, vcc
	global_load_dwordx4 v[14:17], v[2:3], off nt
	s_nop 1
	global_load_dwordx4 v[2:5], v[4:5], off offset:3072 nt
	v_add_co_u32_e32 v8, vcc, 0x52000, v6
	s_nop 1
	v_addc_co_u32_e32 v9, vcc, 0, v7, vcc
	v_add_co_u32_e32 v6, vcc, 0x55000, v6
	s_nop 1
	v_addc_co_u32_e32 v7, vcc, 0, v7, vcc
	global_load_dwordx4 v[18:21], v[8:9], off offset:2048 nt
	s_nop 1
	global_load_dwordx4 v[6:9], v[6:7], off offset:1024 nt
	s_nop 1
	s_waitcnt vmcnt(32)
	ds_bpermute_b32 v86, v141, v89
	s_nop 1
	ds_bpermute_b32 v116, v142, v89
	s_nop 0
	s_waitcnt lgkmcnt(1)
	v_mul_f32_e32 v86, s14, v86
	s_nop 1
	ds_bpermute_b32 v136, v152, v89
	s_nop 0
	s_nop 1
	ds_bpermute_b32 v177, v153, v89
	s_nop 0
	s_nop 1
	s_lshl_b32 s22, s22, 2
	s_nop 0
	s_nop 1
	s_xor_b64 s[18:19], s[18:19], -1
	s_nop 0
	s_waitcnt vmcnt(31)
	v_pk_mul_f32 v[114:115], v[94:95], v[86:87] op_sel_hi:[1,0]
	s_nop 1
	ds_bpermute_b32 v94, v143, v89
	s_nop 0
	s_nop 1
	v_pk_mul_f32 v[92:93], v[96:97], v[86:87] op_sel_hi:[1,0]
	s_nop 0
	s_waitcnt lgkmcnt(3)
	v_mul_f32_e32 v86, s14, v116
	s_waitcnt vmcnt(30)
	v_pk_mul_f32 v[118:119], v[98:99], v[86:87] op_sel_hi:[1,0]
	s_nop 1
	ds_bpermute_b32 v98, v144, v89
	s_nop 0
	s_nop 1
	v_pk_mul_f32 v[96:97], v[100:101], v[86:87] op_sel_hi:[1,0]
	s_nop 0
	s_nop 1
	ds_bpermute_b32 v100, v145, v89
	s_nop 0
	s_waitcnt lgkmcnt(2)
	v_mul_f32_e32 v86, s14, v94
	s_waitcnt vmcnt(29)
	v_pk_mul_f32 v[116:117], v[102:103], v[86:87] op_sel_hi:[1,0]
	s_nop 1
	ds_bpermute_b32 v102, v146, v89
	s_nop 0
	s_nop 1
	v_pk_mul_f32 v[94:95], v[104:105], v[86:87] op_sel_hi:[1,0]
	s_nop 0
	s_waitcnt lgkmcnt(2)
	v_mul_f32_e32 v86, s14, v98
	s_nop 1
	ds_bpermute_b32 v104, v147, v89
	s_nop 0
	s_waitcnt vmcnt(28)
	v_pk_mul_f32 v[120:121], v[106:107], v[86:87] op_sel_hi:[1,0]
	s_nop 1
	ds_bpermute_b32 v106, v148, v89
	s_nop 0
	s_nop 1
	v_pk_mul_f32 v[98:99], v[108:109], v[86:87] op_sel_hi:[1,0]
	s_nop 0
	s_waitcnt lgkmcnt(3)
	v_mul_f32_e32 v86, s14, v100
	s_nop 1
	ds_bpermute_b32 v108, v149, v89
	s_nop 0
	s_waitcnt vmcnt(27)
	v_pk_mul_f32 v[122:123], v[110:111], v[86:87] op_sel_hi:[1,0]
	s_nop 1
	ds_bpermute_b32 v110, v150, v89
	s_nop 0
	s_nop 1
	v_pk_mul_f32 v[100:101], v[112:113], v[86:87] op_sel_hi:[1,0]
	s_nop 0
	s_nop 0
	s_waitcnt lgkmcnt(4)
	v_mul_f32_e32 v86, s14, v102
	s_nop 1
	ds_bpermute_b32 v112, v151, v89
	s_nop 0
	s_nop 0
	s_waitcnt vmcnt(26)
	v_pk_mul_f32 v[102:103], v[126:127], v[86:87] op_sel_hi:[1,0]
	v_pk_mul_f32 v[124:125], v[124:125], v[86:87] op_sel_hi:[1,0]
	s_waitcnt lgkmcnt(4)
	v_mul_f32_e32 v86, s14, v104
	s_waitcnt vmcnt(25)
	v_pk_mul_f32 v[104:105], v[130:131], v[86:87] op_sel_hi:[1,0]
	v_pk_mul_f32 v[126:127], v[128:129], v[86:87] op_sel_hi:[1,0]
	s_waitcnt lgkmcnt(3)
	v_mul_f32_e32 v86, s14, v106
	s_waitcnt vmcnt(24)
	v_pk_mul_f32 v[106:107], v[134:135], v[86:87] op_sel_hi:[1,0]
	v_pk_mul_f32 v[128:129], v[132:133], v[86:87] op_sel_hi:[1,0]
	s_waitcnt lgkmcnt(2)
	v_mul_f32_e32 v86, s14, v108
	s_waitcnt vmcnt(23)
	v_pk_mul_f32 v[108:109], v[180:181], v[86:87] op_sel_hi:[1,0]
	v_pk_mul_f32 v[130:131], v[178:179], v[86:87] op_sel_hi:[1,0]
	s_waitcnt lgkmcnt(1)
	v_mul_f32_e32 v86, s14, v110
	s_waitcnt vmcnt(22)
	v_pk_mul_f32 v[110:111], v[184:185], v[86:87] op_sel_hi:[1,0]
	v_pk_mul_f32 v[132:133], v[182:183], v[86:87] op_sel_hi:[1,0]
	s_waitcnt lgkmcnt(0)
	v_mul_f32_e32 v86, s14, v112
	s_waitcnt vmcnt(21)
	v_pk_mul_f32 v[112:113], v[188:189], v[86:87] op_sel_hi:[1,0]
	v_pk_mul_f32 v[134:135], v[186:187], v[86:87] op_sel_hi:[1,0]
	v_mul_f32_e32 v86, s14, v136
	s_waitcnt vmcnt(20)
	v_pk_mul_f32 v[80:81], v[80:81], v[86:87] op_sel_hi:[1,0]
	v_pk_mul_f32 v[136:137], v[78:79], v[86:87] op_sel_hi:[1,0]
	v_mul_f32_e32 v86, s14, v177
	ds_bpermute_b32 v178, v154, v89
	s_waitcnt vmcnt(19)
	v_pk_mul_f32 v[78:79], v[84:85], v[86:87] op_sel_hi:[1,0]
	v_pk_mul_f32 v[82:83], v[82:83], v[86:87] op_sel_hi:[1,0]
	ds_bpermute_b32 v86, v155, v89
	ds_bpermute_b32 v177, v156, v89
	s_waitcnt lgkmcnt(2)
	v_mul_f32_e32 v84, s14, v178
	s_waitcnt vmcnt(18)
	v_pk_mul_f32 v[72:73], v[72:73], v[84:85] op_sel_hi:[1,0]
	v_pk_mul_f32 v[84:85], v[70:71], v[84:85] op_sel_hi:[1,0]
	s_waitcnt lgkmcnt(1)
	v_mul_f32_e32 v86, s14, v86
	s_waitcnt vmcnt(17)
	v_pk_mul_f32 v[70:71], v[76:77], v[86:87] op_sel_hi:[1,0]
	v_pk_mul_f32 v[74:75], v[74:75], v[86:87] op_sel_hi:[1,0]
	ds_bpermute_b32 v86, v157, v89
	s_waitcnt lgkmcnt(1)
	v_mul_f32_e32 v76, s14, v177
	s_waitcnt vmcnt(16)
	v_pk_mul_f32 v[64:65], v[64:65], v[76:77] op_sel_hi:[1,0]
	v_pk_mul_f32 v[76:77], v[62:63], v[76:77] op_sel_hi:[1,0]
	ds_bpermute_b32 v177, v158, v89
	s_waitcnt lgkmcnt(1)
	v_mul_f32_e32 v86, s14, v86
	s_waitcnt vmcnt(15)
	v_pk_mul_f32 v[62:63], v[68:69], v[86:87] op_sel_hi:[1,0]
	v_pk_mul_f32 v[66:67], v[66:67], v[86:87] op_sel_hi:[1,0]
	ds_bpermute_b32 v86, v159, v89
	s_waitcnt lgkmcnt(1)
	v_mul_f32_e32 v68, s14, v177
	s_waitcnt vmcnt(14)
	v_pk_mul_f32 v[56:57], v[56:57], v[68:69] op_sel_hi:[1,0]
	v_pk_mul_f32 v[68:69], v[54:55], v[68:69] op_sel_hi:[1,0]
	ds_bpermute_b32 v177, v160, v89
	s_waitcnt lgkmcnt(1)
	v_mul_f32_e32 v86, s14, v86
	s_waitcnt vmcnt(13)
	v_pk_mul_f32 v[54:55], v[60:61], v[86:87] op_sel_hi:[1,0]
	v_pk_mul_f32 v[58:59], v[58:59], v[86:87] op_sel_hi:[1,0]
	ds_bpermute_b32 v86, v161, v89
	s_waitcnt lgkmcnt(1)
	v_mul_f32_e32 v60, s14, v177
	s_waitcnt vmcnt(12)
	v_pk_mul_f32 v[48:49], v[48:49], v[60:61] op_sel_hi:[1,0]
	v_pk_mul_f32 v[60:61], v[46:47], v[60:61] op_sel_hi:[1,0]
	ds_bpermute_b32 v177, v162, v89
	s_waitcnt lgkmcnt(1)
	v_mul_f32_e32 v86, s14, v86
	s_waitcnt vmcnt(11)
	v_pk_mul_f32 v[46:47], v[52:53], v[86:87] op_sel_hi:[1,0]
	v_pk_mul_f32 v[50:51], v[50:51], v[86:87] op_sel_hi:[1,0]
	ds_bpermute_b32 v86, v163, v89
	s_waitcnt lgkmcnt(1)
	v_mul_f32_e32 v52, s14, v177
	s_waitcnt vmcnt(10)
	v_pk_mul_f32 v[40:41], v[40:41], v[52:53] op_sel_hi:[1,0]
	v_pk_mul_f32 v[52:53], v[38:39], v[52:53] op_sel_hi:[1,0]
	ds_bpermute_b32 v177, v164, v89
	s_waitcnt lgkmcnt(1)
	v_mul_f32_e32 v86, s14, v86
	s_waitcnt vmcnt(9)
	v_pk_mul_f32 v[38:39], v[44:45], v[86:87] op_sel_hi:[1,0]
	v_pk_mul_f32 v[42:43], v[42:43], v[86:87] op_sel_hi:[1,0]
	ds_bpermute_b32 v86, v165, v89
	s_waitcnt lgkmcnt(1)
	v_mul_f32_e32 v44, s14, v177
	ds_bpermute_b32 v177, v167, v89
	s_waitcnt vmcnt(8)
	v_pk_mul_f32 v[32:33], v[32:33], v[44:45] op_sel_hi:[1,0]
	v_pk_mul_f32 v[44:45], v[30:31], v[44:45] op_sel_hi:[1,0]
	s_waitcnt lgkmcnt(1)
	v_mul_f32_e32 v86, s14, v86
	s_waitcnt vmcnt(7)
	v_pk_mul_f32 v[30:31], v[36:37], v[86:87] op_sel_hi:[1,0]
	ds_bpermute_b32 v37, v168, v89
	v_pk_mul_f32 v[34:35], v[34:35], v[86:87] op_sel_hi:[1,0]
	ds_bpermute_b32 v86, v169, v89
	s_waitcnt lgkmcnt(2)
	v_mul_f32_e32 v36, s14, v177
	ds_bpermute_b32 v177, v170, v89
	s_waitcnt vmcnt(6) lgkmcnt(2)
	v_pk_mul_f32 v[24:25], v[24:25], v[36:37] op_sel_hi:[1,0]
	v_pk_mul_f32 v[22:23], v[22:23], v[36:37] op_sel_hi:[1,0]
	v_mul_f32_e32 v36, s14, v37
	s_waitcnt vmcnt(5)
	v_pk_mul_f32 v[28:29], v[28:29], v[36:37] op_sel_hi:[1,0]
	v_pk_mul_f32 v[26:27], v[26:27], v[36:37] op_sel_hi:[1,0]
	s_waitcnt lgkmcnt(1)
	v_mul_f32_e32 v36, s14, v86
	s_waitcnt vmcnt(4)
	v_pk_mul_f32 v[178:179], v[12:13], v[36:37] op_sel_hi:[1,0]
	v_pk_mul_f32 v[36:37], v[10:11], v[36:37] op_sel_hi:[1,0]
	ds_bpermute_b32 v11, v171, v89
	s_waitcnt lgkmcnt(1)
	v_mul_f32_e32 v10, s14, v177
	ds_bpermute_b32 v12, v172, v89
	v_mov_b32_e32 v13, v87
	s_andn2_b64 vcc, exec, s[18:19]
	s_waitcnt vmcnt(3) lgkmcnt(1)
	v_pk_mul_f32 v[180:181], v[16:17], v[10:11] op_sel_hi:[1,0]
	v_pk_mul_f32 v[14:15], v[14:15], v[10:11] op_sel_hi:[1,0]
	v_mul_f32_e32 v10, s14, v11
	s_waitcnt vmcnt(2)
	v_pk_mul_f32 v[182:183], v[4:5], v[10:11] op_sel_hi:[1,0]
	ds_bpermute_b32 v4, v173, v89
	v_pk_mul_f32 v[16:17], v[2:3], v[10:11] op_sel_hi:[1,0]
	s_waitcnt lgkmcnt(1)
	v_mul_f32_e32 v2, s14, v12
	s_waitcnt vmcnt(1)
	v_pk_mul_f32 v[20:21], v[20:21], v[2:3] op_sel_hi:[1,0]
	v_pk_mul_f32 v[18:19], v[18:19], v[2:3] op_sel_hi:[1,0]
	s_waitcnt lgkmcnt(0)
	v_mul_f32_e32 v2, s14, v4
	s_waitcnt vmcnt(0)
	v_pk_mul_f32 v[184:185], v[8:9], v[2:3] op_sel_hi:[1,0]
	v_pk_mul_f32 v[186:187], v[6:7], v[2:3] op_sel_hi:[1,0]
	v_mov_b32_e32 v2, v87
	v_mov_b32_e32 v3, v87
	v_mov_b32_e32 v4, v87
	v_mov_b32_e32 v5, v87
	v_cvt_pk_fp8_f32 v2, v114, v118
	v_cvt_pk_fp8_f32 v3, v122, v124
	v_cvt_pk_fp8_f32 v4, v130, v132
	v_cvt_pk_fp8_f32 v5, v82, v84
	v_cvt_pk_fp8_f32 v2, v116, v120 op_sel:[0,0,1]
	v_cvt_pk_fp8_f32 v3, v126, v128 op_sel:[0,0,1]
	v_cvt_pk_fp8_f32 v4, v134, v136 op_sel:[0,0,1]
	v_cvt_pk_fp8_f32 v5, v74, v76 op_sel:[0,0,1]
	v_bitop3_b32 v7, s22, v140, v139 bitop3:0x36
	v_lshl_add_u32 v74, v7, 4, v174
	v_or_b32_e32 v6, s22, v139
	ds_write_b128 v74, v[2:5]
	v_mov_b32_e32 v2, v87
	v_mov_b32_e32 v3, v87
	v_mov_b32_e32 v4, v87
	v_mov_b32_e32 v5, v87
	v_cvt_pk_fp8_f32 v2, v66, v68
	v_cvt_pk_fp8_f32 v3, v50, v52
	v_cvt_pk_fp8_f32 v4, v34, v22
	v_cvt_pk_fp8_f32 v5, v14, v16
	v_bitop3_b32 v14, v6, v140, 1 bitop3:0x36
	v_mov_b32_e32 v6, v87
	v_mov_b32_e32 v7, v87
	v_mov_b32_e32 v8, v87
	v_mov_b32_e32 v9, v87
	v_cvt_pk_fp8_f32 v6, v115, v119
	v_cvt_pk_fp8_f32 v7, v123, v125
	v_cvt_pk_fp8_f32 v8, v131, v133
	v_cvt_pk_fp8_f32 v9, v83, v85
	v_mov_b32_e32 v10, v87
	v_mov_b32_e32 v11, v87
	v_mov_b32_e32 v12, v87
	v_cvt_pk_fp8_f32 v10, v67, v69
	v_cvt_pk_fp8_f32 v11, v51, v53
	v_cvt_pk_fp8_f32 v12, v35, v23
	v_cvt_pk_fp8_f32 v13, v15, v17
	v_cvt_pk_fp8_f32 v2, v58, v60 op_sel:[0,0,1]
	v_cvt_pk_fp8_f32 v3, v42, v44 op_sel:[0,0,1]
	v_cvt_pk_fp8_f32 v4, v26, v36 op_sel:[0,0,1]
	v_cvt_pk_fp8_f32 v5, v18, v186 op_sel:[0,0,1]
	v_cvt_pk_fp8_f32 v6, v117, v121 op_sel:[0,0,1]
	v_cvt_pk_fp8_f32 v7, v127, v129 op_sel:[0,0,1]
	v_cvt_pk_fp8_f32 v8, v135, v137 op_sel:[0,0,1]
	v_cvt_pk_fp8_f32 v9, v75, v77 op_sel:[0,0,1]
	v_cvt_pk_fp8_f32 v10, v59, v61 op_sel:[0,0,1]
	v_cvt_pk_fp8_f32 v11, v43, v45 op_sel:[0,0,1]
	v_cvt_pk_fp8_f32 v12, v27, v37 op_sel:[0,0,1]
	v_cvt_pk_fp8_f32 v13, v19, v187 op_sel:[0,0,1]
	v_lshl_add_u32 v18, v14, 4, v174
	ds_write_b128 v18, v[2:5]
	ds_write_b128 v74, v[6:9] offset:128
	ds_write_b128 v18, v[10:13] offset:128
	v_mov_b32_e32 v2, v87
	v_mov_b32_e32 v3, v87
	v_mov_b32_e32 v4, v87
	v_mov_b32_e32 v5, v87
	v_cvt_pk_fp8_f32 v2, v92, v96
	v_cvt_pk_fp8_f32 v3, v100, v102
	v_cvt_pk_fp8_f32 v4, v108, v110
	v_cvt_pk_fp8_f32 v5, v78, v72
	v_mov_b32_e32 v6, v87
	v_mov_b32_e32 v7, v87
	v_mov_b32_e32 v8, v87
	v_mov_b32_e32 v9, v87
	v_cvt_pk_fp8_f32 v6, v62, v56
	v_cvt_pk_fp8_f32 v7, v46, v40
	v_cvt_pk_fp8_f32 v8, v30, v24
	v_cvt_pk_fp8_f32 v9, v180, v182
	v_mov_b32_e32 v10, v87
	v_mov_b32_e32 v11, v87
	v_mov_b32_e32 v12, v87
	v_mov_b32_e32 v13, v87
	v_cvt_pk_fp8_f32 v10, v93, v97
	v_cvt_pk_fp8_f32 v11, v101, v103
	v_cvt_pk_fp8_f32 v12, v109, v111
	v_cvt_pk_fp8_f32 v13, v79, v73
	v_mov_b32_e32 v14, v87
	v_mov_b32_e32 v15, v87
	v_mov_b32_e32 v16, v87
	v_mov_b32_e32 v17, v87
	v_cvt_pk_fp8_f32 v14, v63, v57
	v_cvt_pk_fp8_f32 v15, v47, v41
	v_cvt_pk_fp8_f32 v16, v31, v25
	v_cvt_pk_fp8_f32 v17, v181, v183
	v_cvt_pk_fp8_f32 v2, v94, v98 op_sel:[0,0,1]
	v_cvt_pk_fp8_f32 v3, v104, v106 op_sel:[0,0,1]
	v_cvt_pk_fp8_f32 v4, v112, v80 op_sel:[0,0,1]
	v_cvt_pk_fp8_f32 v5, v70, v64 op_sel:[0,0,1]
	v_cvt_pk_fp8_f32 v6, v54, v48 op_sel:[0,0,1]
	v_cvt_pk_fp8_f32 v7, v38, v32 op_sel:[0,0,1]
	v_cvt_pk_fp8_f32 v8, v28, v178 op_sel:[0,0,1]
	v_cvt_pk_fp8_f32 v9, v20, v184 op_sel:[0,0,1]
	v_cvt_pk_fp8_f32 v10, v95, v99 op_sel:[0,0,1]
	v_cvt_pk_fp8_f32 v11, v105, v107 op_sel:[0,0,1]
	v_cvt_pk_fp8_f32 v12, v113, v81 op_sel:[0,0,1]
	v_cvt_pk_fp8_f32 v13, v71, v65 op_sel:[0,0,1]
	s_mov_b32 s22, 1
	v_cvt_pk_fp8_f32 v14, v55, v49 op_sel:[0,0,1]
	v_cvt_pk_fp8_f32 v15, v39, v33 op_sel:[0,0,1]
	v_cvt_pk_fp8_f32 v16, v29, v179 op_sel:[0,0,1]
	v_cvt_pk_fp8_f32 v17, v21, v185 op_sel:[0,0,1]
	s_mov_b64 s[18:19], 0
	ds_write_b128 v74, v[2:5] offset:256
	ds_write_b128 v18, v[6:9] offset:256
	ds_write_b128 v74, v[10:13] offset:384
	ds_write_b128 v18, v[14:17] offset:384
	s_cbranch_vccz .LBB0_71

.Lfret_1:
	s_mov_b32 s101, 0
	s_waitcnt lgkmcnt(0)
	s_barrier
